# all per-phase s_setprio flips in the GEMM loops deleted (no static priority)
# speedup vs baseline: 1.0082x; 1.0082x over previous
.Lpg8f0:
	s_waitcnt lgkmcnt(0)
	s_barrier
	s_waitcnt lgkmcnt(0)
	v_mfma_f32_16x16x32_bf16 v[84:87], v[148:151], v[198:201], v[84:87]
	v_mfma_f32_16x16x32_bf16 v[144:147], v[156:159], v[198:201], v[144:147]
	v_mfma_f32_16x16x32_bf16 v[140:143], v[148:151], v[206:209], v[140:143]
	v_mfma_f32_16x16x32_bf16 v[136:139], v[156:159], v[206:209], v[136:139]
	v_mfma_f32_16x16x32_bf16 v[132:135], v[148:151], v[226:229], v[132:135]
	v_mfma_f32_16x16x32_bf16 v[128:131], v[156:159], v[226:229], v[128:131]
	v_mfma_f32_16x16x32_bf16 v[124:127], v[148:151], v[240:243], v[124:127]
	v_mfma_f32_16x16x32_bf16 v[120:123], v[156:159], v[240:243], v[120:123]
	v_mfma_f32_16x16x32_bf16 v[84:87], v[152:155], v[202:205], v[84:87]
	v_mfma_f32_16x16x32_bf16 v[144:147], v[160:163], v[202:205], v[144:147]
	v_mfma_f32_16x16x32_bf16 v[140:143], v[152:155], v[222:225], v[140:143]
	v_mfma_f32_16x16x32_bf16 v[136:139], v[160:163], v[222:225], v[136:139]
	v_mfma_f32_16x16x32_bf16 v[132:135], v[152:155], v[236:239], v[132:135]
	v_mfma_f32_16x16x32_bf16 v[128:131], v[160:163], v[236:239], v[128:131]
	v_mfma_f32_16x16x32_bf16 v[124:127], v[152:155], v[244:247], v[124:127]
	v_mfma_f32_16x16x32_bf16 v[120:123], v[160:163], v[244:247], v[120:123]
	v_mfma_f32_16x16x32_bf16 v[116:119], v[164:167], v[198:201], v[116:119]
	v_mfma_f32_16x16x32_bf16 v[112:115], v[184:187], v[198:201], v[112:115]
	v_mfma_f32_16x16x32_bf16 v[108:111], v[164:167], v[206:209], v[108:111]
	v_mfma_f32_16x16x32_bf16 v[104:107], v[184:187], v[206:209], v[104:107]
	v_mfma_f32_16x16x32_bf16 v[100:103], v[164:167], v[226:229], v[100:103]
	v_mfma_f32_16x16x32_bf16 v[96:99], v[184:187], v[226:229], v[96:99]
	v_mfma_f32_16x16x32_bf16 v[92:95], v[164:167], v[240:243], v[92:95]
	v_mfma_f32_16x16x32_bf16 v[88:91], v[184:187], v[240:243], v[88:91]
	v_mfma_f32_16x16x32_bf16 v[116:119], v[180:183], v[202:205], v[116:119]
	v_mfma_f32_16x16x32_bf16 v[112:115], v[188:191], v[202:205], v[112:115]
	v_mfma_f32_16x16x32_bf16 v[108:111], v[180:183], v[222:225], v[108:111]
	v_mfma_f32_16x16x32_bf16 v[104:107], v[188:191], v[222:225], v[104:107]
	v_mfma_f32_16x16x32_bf16 v[100:103], v[180:183], v[236:239], v[100:103]
	v_mfma_f32_16x16x32_bf16 v[96:99], v[188:191], v[236:239], v[96:99]
	v_mfma_f32_16x16x32_bf16 v[92:95], v[180:183], v[244:247], v[92:95]
	v_mfma_f32_16x16x32_bf16 v[88:91], v[188:191], v[244:247], v[88:91]
	s_barrier
	s_mov_b32 m0, s54
	v_lshl_add_u64 v[210:211], s[42:43], 0, v[170:171]
	s_add_u32 s50, s42, 0x40000
	ds_read_b128 v[198:201], v219 offset:16384
	ds_read_b128 v[202:205], v219 offset:17408
	ds_read_b128 v[206:209], v219 offset:18432
	ds_read_b128 v[222:225], v219 offset:19456
	ds_read_b128 v[226:229], v219 offset:20480
	ds_read_b128 v[236:239], v219 offset:21504
	ds_read_b128 v[240:243], v219 offset:22528
	ds_read_b128 v[244:247], v219 offset:23552
	global_load_lds_dwordx4 v[210:211], off
	v_lshl_add_u64 v[230:231], s[42:43], 0, v[174:175]
	s_mov_b32 m0, s83
	s_addc_u32 s51, s43, 0
	global_load_lds_dwordx4 v[230:231], off
	v_lshl_add_u64 v[248:249], s[50:51], 0, v[170:171]
	s_mov_b32 m0, s26
	v_lshl_add_u64 v[250:251], s[22:23], 0, v[172:173]
	global_load_lds_dwordx4 v[248:249], off
	v_lshl_add_u64 v[248:249], s[50:51], 0, v[174:175]
	s_mov_b32 m0, s27
	s_nop 0
	global_load_lds_dwordx4 v[248:249], off
	v_lshl_add_u64 v[248:249], s[22:23], 0, v[168:169]
	s_mov_b32 m0, s44
	s_nop 0
	global_load_lds_dwordx4 v[248:249], off
	s_mov_b32 m0, s81
	s_nop 0
	global_load_lds_dwordx4 v[250:251], off
	s_waitcnt vmcnt(24)
	s_cmp_lg_u32 s53, 0
	s_cbranch_scc1 .Lpg8f1
	s_waitcnt vmcnt(8)
.Lpg8f1:
	s_waitcnt lgkmcnt(0)
	s_barrier
	s_waitcnt lgkmcnt(0)
	v_mfma_f32_16x16x32_bf16 v[80:83], v[148:151], v[198:201], v[80:83]
	v_mfma_f32_16x16x32_bf16 v[76:79], v[156:159], v[198:201], v[76:79]
	v_mfma_f32_16x16x32_bf16 v[72:75], v[148:151], v[206:209], v[72:75]
	v_mfma_f32_16x16x32_bf16 v[68:71], v[156:159], v[206:209], v[68:71]
	v_mfma_f32_16x16x32_bf16 v[64:67], v[148:151], v[226:229], v[64:67]
	v_mfma_f32_16x16x32_bf16 v[60:63], v[156:159], v[226:229], v[60:63]
	v_mfma_f32_16x16x32_bf16 v[56:59], v[148:151], v[240:243], v[56:59]
	v_mfma_f32_16x16x32_bf16 v[52:55], v[156:159], v[240:243], v[52:55]
	v_mfma_f32_16x16x32_bf16 v[80:83], v[152:155], v[202:205], v[80:83]
	v_mfma_f32_16x16x32_bf16 v[76:79], v[160:163], v[202:205], v[76:79]
	v_mfma_f32_16x16x32_bf16 v[72:75], v[152:155], v[222:225], v[72:75]
	v_mfma_f32_16x16x32_bf16 v[68:71], v[160:163], v[222:225], v[68:71]
	v_mfma_f32_16x16x32_bf16 v[64:67], v[152:155], v[236:239], v[64:67]
	v_mfma_f32_16x16x32_bf16 v[60:63], v[160:163], v[236:239], v[60:63]
	v_mfma_f32_16x16x32_bf16 v[56:59], v[152:155], v[244:247], v[56:59]
	v_mfma_f32_16x16x32_bf16 v[52:55], v[160:163], v[244:247], v[52:55]
	v_mfma_f32_16x16x32_bf16 v[48:51], v[164:167], v[198:201], v[48:51]
	v_mfma_f32_16x16x32_bf16 v[44:47], v[184:187], v[198:201], v[44:47]
	v_mfma_f32_16x16x32_bf16 v[40:43], v[164:167], v[206:209], v[40:43]
	v_mfma_f32_16x16x32_bf16 v[36:39], v[184:187], v[206:209], v[36:39]
	v_mfma_f32_16x16x32_bf16 v[32:35], v[164:167], v[226:229], v[32:35]
	v_mfma_f32_16x16x32_bf16 v[28:31], v[184:187], v[226:229], v[28:31]
	v_mfma_f32_16x16x32_bf16 v[24:27], v[164:167], v[240:243], v[24:27]
	v_mfma_f32_16x16x32_bf16 v[20:23], v[184:187], v[240:243], v[20:23]
	v_mfma_f32_16x16x32_bf16 v[48:51], v[180:183], v[202:205], v[48:51]
	v_mfma_f32_16x16x32_bf16 v[44:47], v[188:191], v[202:205], v[44:47]
	v_mfma_f32_16x16x32_bf16 v[40:43], v[180:183], v[222:225], v[40:43]
	v_mfma_f32_16x16x32_bf16 v[36:39], v[188:191], v[222:225], v[36:39]
	v_mfma_f32_16x16x32_bf16 v[32:35], v[180:183], v[236:239], v[32:35]
	v_mfma_f32_16x16x32_bf16 v[28:31], v[188:191], v[236:239], v[28:31]
	v_mfma_f32_16x16x32_bf16 v[24:27], v[180:183], v[244:247], v[24:27]
	v_mfma_f32_16x16x32_bf16 v[20:23], v[188:191], v[244:247], v[20:23]
	s_barrier
	v_add_u32_e32 v160, s61, v215
	v_add_u32_e32 v188, s70, v215
	ds_read_b128 v[148:151], v160
	ds_read_b128 v[152:155], v160 offset:1024
	ds_read_b128 v[156:159], v160 offset:2048
	ds_read_b128 v[160:163], v160 offset:3072
	ds_read_b128 v[164:167], v188
	ds_read_b128 v[180:183], v188 offset:1024
	ds_read_b128 v[184:187], v188 offset:2048
	ds_read_b128 v[188:191], v188 offset:3072
	s_add_u32 s50, s22, 0x40000
	s_addc_u32 s51, s23, 0
	s_mov_b32 m0, s91
	v_lshl_add_u64 v[252:253], s[50:51], 0, v[168:169]
	ds_read_b128 v[198:201], v219 offset:32768
	ds_read_b128 v[202:205], v219 offset:33792
	ds_read_b128 v[206:209], v219 offset:34816
	ds_read_b128 v[222:225], v219 offset:35840
	ds_read_b128 v[226:229], v219 offset:36864
	ds_read_b128 v[236:239], v219 offset:37888
	ds_read_b128 v[240:243], v219 offset:38912
	ds_read_b128 v[244:247], v219 offset:39936
	global_load_lds_dwordx4 v[252:253], off
	v_lshl_add_u64 v[252:253], s[50:51], 0, v[172:173]
	s_mov_b32 m0, s33
	s_nop 0
	global_load_lds_dwordx4 v[252:253], off
	s_waitcnt vmcnt(24)
	s_cmp_lg_u32 s53, 0
	s_cbranch_scc1 .Lpg8f2
	s_waitcnt vmcnt(8)
.Lpg8f2:
	s_waitcnt lgkmcnt(0)
	s_barrier
	s_waitcnt lgkmcnt(0)
	v_mfma_f32_16x16x32_bf16 v[84:87], v[148:151], v[198:201], v[84:87]
	v_mfma_f32_16x16x32_bf16 v[144:147], v[156:159], v[198:201], v[144:147]
	v_mfma_f32_16x16x32_bf16 v[140:143], v[148:151], v[206:209], v[140:143]
	v_mfma_f32_16x16x32_bf16 v[136:139], v[156:159], v[206:209], v[136:139]
	v_mfma_f32_16x16x32_bf16 v[132:135], v[148:151], v[226:229], v[132:135]
	v_mfma_f32_16x16x32_bf16 v[128:131], v[156:159], v[226:229], v[128:131]
	v_mfma_f32_16x16x32_bf16 v[124:127], v[148:151], v[240:243], v[124:127]
	v_mfma_f32_16x16x32_bf16 v[120:123], v[156:159], v[240:243], v[120:123]
	v_mfma_f32_16x16x32_bf16 v[84:87], v[152:155], v[202:205], v[84:87]
	v_mfma_f32_16x16x32_bf16 v[144:147], v[160:163], v[202:205], v[144:147]
	v_mfma_f32_16x16x32_bf16 v[140:143], v[152:155], v[222:225], v[140:143]
	v_mfma_f32_16x16x32_bf16 v[136:139], v[160:163], v[222:225], v[136:139]
	v_mfma_f32_16x16x32_bf16 v[132:135], v[152:155], v[236:239], v[132:135]
	v_mfma_f32_16x16x32_bf16 v[128:131], v[160:163], v[236:239], v[128:131]
	v_mfma_f32_16x16x32_bf16 v[124:127], v[152:155], v[244:247], v[124:127]
	v_mfma_f32_16x16x32_bf16 v[120:123], v[160:163], v[244:247], v[120:123]
	v_mfma_f32_16x16x32_bf16 v[116:119], v[164:167], v[198:201], v[116:119]
	v_mfma_f32_16x16x32_bf16 v[112:115], v[184:187], v[198:201], v[112:115]
	v_mfma_f32_16x16x32_bf16 v[108:111], v[164:167], v[206:209], v[108:111]
	v_mfma_f32_16x16x32_bf16 v[104:107], v[184:187], v[206:209], v[104:107]
	v_mfma_f32_16x16x32_bf16 v[100:103], v[164:167], v[226:229], v[100:103]
	v_mfma_f32_16x16x32_bf16 v[96:99], v[184:187], v[226:229], v[96:99]
	v_mfma_f32_16x16x32_bf16 v[92:95], v[164:167], v[240:243], v[92:95]
	v_mfma_f32_16x16x32_bf16 v[88:91], v[184:187], v[240:243], v[88:91]
	v_mfma_f32_16x16x32_bf16 v[116:119], v[180:183], v[202:205], v[116:119]
	v_mfma_f32_16x16x32_bf16 v[112:115], v[188:191], v[202:205], v[112:115]
	v_mfma_f32_16x16x32_bf16 v[108:111], v[180:183], v[222:225], v[108:111]
	v_mfma_f32_16x16x32_bf16 v[104:107], v[188:191], v[222:225], v[104:107]
	v_mfma_f32_16x16x32_bf16 v[100:103], v[180:183], v[236:239], v[100:103]
	v_mfma_f32_16x16x32_bf16 v[96:99], v[188:191], v[236:239], v[96:99]
	v_mfma_f32_16x16x32_bf16 v[92:95], v[180:183], v[244:247], v[92:95]
	v_mfma_f32_16x16x32_bf16 v[88:91], v[188:191], v[244:247], v[88:91]
	s_barrier
	s_mov_b32 m0, s46
	v_lshl_add_u64 v[210:211], v[210:211], 0, s[86:87]
	s_add_u32 s42, s42, 0x40080
	ds_read_b128 v[198:201], v219 offset:49152
	ds_read_b128 v[202:205], v219 offset:50176
	ds_read_b128 v[206:209], v219 offset:51200
	ds_read_b128 v[222:225], v219 offset:52224
	ds_read_b128 v[226:229], v219 offset:53248
	ds_read_b128 v[236:239], v219 offset:54272
	ds_read_b128 v[240:243], v219 offset:55296
	ds_read_b128 v[244:247], v219 offset:56320
	global_load_lds_dwordx4 v[210:211], off
	v_lshl_add_u64 v[210:211], v[230:231], 0, s[86:87]
	s_mov_b32 m0, s47
	s_addc_u32 s43, s43, 0
	global_load_lds_dwordx4 v[210:211], off
	v_lshl_add_u64 v[210:211], s[42:43], 0, v[170:171]
	s_mov_b32 m0, s71
	s_nop 0
	global_load_lds_dwordx4 v[210:211], off
	v_lshl_add_u64 v[210:211], s[42:43], 0, v[174:175]
	s_mov_b32 m0, s24
	s_nop 0
	global_load_lds_dwordx4 v[210:211], off
	v_lshl_add_u64 v[210:211], v[248:249], 0, s[86:87]
	s_mov_b32 m0, s80
	s_nop 0
	global_load_lds_dwordx4 v[210:211], off
	v_lshl_add_u64 v[210:211], v[250:251], 0, s[86:87]
	s_mov_b32 m0, s67
	s_nop 0
	global_load_lds_dwordx4 v[210:211], off
	s_waitcnt vmcnt(8)
	s_waitcnt lgkmcnt(0)
	s_barrier
	s_waitcnt lgkmcnt(0)
	v_mfma_f32_16x16x32_bf16 v[80:83], v[148:151], v[198:201], v[80:83]
	v_mfma_f32_16x16x32_bf16 v[76:79], v[156:159], v[198:201], v[76:79]
	v_mfma_f32_16x16x32_bf16 v[72:75], v[148:151], v[206:209], v[72:75]
	v_mfma_f32_16x16x32_bf16 v[68:71], v[156:159], v[206:209], v[68:71]
	v_mfma_f32_16x16x32_bf16 v[64:67], v[148:151], v[226:229], v[64:67]
	v_mfma_f32_16x16x32_bf16 v[60:63], v[156:159], v[226:229], v[60:63]
	v_mfma_f32_16x16x32_bf16 v[56:59], v[148:151], v[240:243], v[56:59]
	v_mfma_f32_16x16x32_bf16 v[52:55], v[156:159], v[240:243], v[52:55]
	v_mfma_f32_16x16x32_bf16 v[80:83], v[152:155], v[202:205], v[80:83]
	v_mfma_f32_16x16x32_bf16 v[76:79], v[160:163], v[202:205], v[76:79]
	v_mfma_f32_16x16x32_bf16 v[72:75], v[152:155], v[222:225], v[72:75]
	v_mfma_f32_16x16x32_bf16 v[68:71], v[160:163], v[222:225], v[68:71]
	v_mfma_f32_16x16x32_bf16 v[64:67], v[152:155], v[236:239], v[64:67]
	v_mfma_f32_16x16x32_bf16 v[60:63], v[160:163], v[236:239], v[60:63]
	v_mfma_f32_16x16x32_bf16 v[56:59], v[152:155], v[244:247], v[56:59]
	v_mfma_f32_16x16x32_bf16 v[52:55], v[160:163], v[244:247], v[52:55]
	v_mfma_f32_16x16x32_bf16 v[48:51], v[164:167], v[198:201], v[48:51]
	v_mfma_f32_16x16x32_bf16 v[44:47], v[184:187], v[198:201], v[44:47]
	v_mfma_f32_16x16x32_bf16 v[40:43], v[164:167], v[206:209], v[40:43]
	v_mfma_f32_16x16x32_bf16 v[36:39], v[184:187], v[206:209], v[36:39]
	v_mfma_f32_16x16x32_bf16 v[32:35], v[164:167], v[226:229], v[32:35]
	v_mfma_f32_16x16x32_bf16 v[28:31], v[184:187], v[226:229], v[28:31]
	v_mfma_f32_16x16x32_bf16 v[24:27], v[164:167], v[240:243], v[24:27]
	v_mfma_f32_16x16x32_bf16 v[20:23], v[184:187], v[240:243], v[20:23]
	v_mfma_f32_16x16x32_bf16 v[48:51], v[180:183], v[202:205], v[48:51]
	v_mfma_f32_16x16x32_bf16 v[44:47], v[188:191], v[202:205], v[44:47]
	v_mfma_f32_16x16x32_bf16 v[40:43], v[180:183], v[222:225], v[40:43]
	v_mfma_f32_16x16x32_bf16 v[36:39], v[188:191], v[222:225], v[36:39]
	v_mfma_f32_16x16x32_bf16 v[32:35], v[180:183], v[236:239], v[32:35]
	v_mfma_f32_16x16x32_bf16 v[28:31], v[188:191], v[236:239], v[28:31]
	v_mfma_f32_16x16x32_bf16 v[24:27], v[180:183], v[244:247], v[24:27]
	v_mfma_f32_16x16x32_bf16 v[20:23], v[188:191], v[244:247], v[20:23]
	s_barrier
	s_add_u32 s22, s22, 0x40080
	s_addc_u32 s23, s23, 0
	s_mov_b32 m0, s25
	v_lshl_add_u64 v[148:149], s[22:23], 0, v[168:169]
	global_load_lds_dwordx4 v[148:149], off
	v_lshl_add_u64 v[148:149], s[22:23], 0, v[172:173]
	s_mov_b32 m0, s66
	s_nop 0
	global_load_lds_dwordx4 v[148:149], off
	s_add_i32 s48, s48, 2
	s_add_u32 s4, s4, 0x100
	s_addc_u32 s5, s5, 0
	s_cmp_gt_u32 s48, 13
	s_cbranch_scc0 .LBB0_403
	s_and_b64 vcc, exec, s[38:39]
	s_cbranch_vccz .LBB0_406
	s_barrier

.Lpg8f3:
	s_waitcnt lgkmcnt(0)
	s_barrier
	s_waitcnt lgkmcnt(0)
	v_mfma_f32_16x16x32_bf16 v[144:147], v[120:123], v[176:179], v[144:147]
	v_mfma_f32_16x16x32_bf16 v[140:143], v[152:155], v[176:179], v[140:143]
	v_mfma_f32_16x16x32_bf16 v[128:131], v[120:123], v[184:187], v[128:131]
	v_mfma_f32_16x16x32_bf16 v[124:127], v[152:155], v[184:187], v[124:127]
	v_mfma_f32_16x16x32_bf16 v[96:99], v[120:123], v[198:201], v[96:99]
	v_mfma_f32_16x16x32_bf16 v[92:95], v[152:155], v[198:201], v[92:95]
	v_mfma_f32_16x16x32_bf16 v[80:83], v[120:123], v[206:209], v[80:83]
	v_mfma_f32_16x16x32_bf16 v[76:79], v[152:155], v[206:209], v[76:79]
	v_mfma_f32_16x16x32_bf16 v[144:147], v[148:151], v[180:183], v[144:147]
	v_mfma_f32_16x16x32_bf16 v[140:143], v[156:159], v[180:183], v[140:143]
	v_mfma_f32_16x16x32_bf16 v[128:131], v[148:151], v[188:191], v[128:131]
	v_mfma_f32_16x16x32_bf16 v[124:127], v[156:159], v[188:191], v[124:127]
	v_mfma_f32_16x16x32_bf16 v[96:99], v[148:151], v[202:205], v[96:99]
	v_mfma_f32_16x16x32_bf16 v[92:95], v[156:159], v[202:205], v[92:95]
	v_mfma_f32_16x16x32_bf16 v[80:83], v[148:151], v[210:213], v[80:83]
	v_mfma_f32_16x16x32_bf16 v[76:79], v[156:159], v[210:213], v[76:79]
	v_mfma_f32_16x16x32_bf16 v[136:139], v[160:163], v[176:179], v[136:139]
	v_mfma_f32_16x16x32_bf16 v[132:135], v[168:171], v[176:179], v[132:135]
	v_mfma_f32_16x16x32_bf16 v[112:115], v[160:163], v[184:187], v[112:115]
	v_mfma_f32_16x16x32_bf16 v[108:111], v[168:171], v[184:187], v[108:111]
	v_mfma_f32_16x16x32_bf16 v[88:91], v[160:163], v[198:201], v[88:91]
	v_mfma_f32_16x16x32_bf16 v[84:87], v[168:171], v[198:201], v[84:87]
	v_mfma_f32_16x16x32_bf16 v[72:75], v[160:163], v[206:209], v[72:75]
	v_mfma_f32_16x16x32_bf16 v[68:71], v[168:171], v[206:209], v[68:71]
	v_mfma_f32_16x16x32_bf16 v[136:139], v[164:167], v[180:183], v[136:139]
	v_mfma_f32_16x16x32_bf16 v[132:135], v[172:175], v[180:183], v[132:135]
	v_mfma_f32_16x16x32_bf16 v[112:115], v[164:167], v[188:191], v[112:115]
	v_mfma_f32_16x16x32_bf16 v[108:111], v[172:175], v[188:191], v[108:111]
	v_mfma_f32_16x16x32_bf16 v[88:91], v[164:167], v[202:205], v[88:91]
	v_mfma_f32_16x16x32_bf16 v[84:87], v[172:175], v[202:205], v[84:87]
	v_mfma_f32_16x16x32_bf16 v[72:75], v[164:167], v[210:213], v[72:75]
	v_mfma_f32_16x16x32_bf16 v[68:71], v[172:175], v[210:213], v[68:71]
	s_barrier
	s_mov_b32 m0, s10
	v_lshl_add_u64 v[214:215], s[34:35], 0, v[2:3]
	v_lshl_add_u64 v[216:217], s[34:35], 0, v[104:105]
	s_add_u32 s34, s34, s82
	ds_read_b128 v[176:179], v118 offset:16384
	ds_read_b128 v[180:183], v118 offset:17408
	ds_read_b128 v[184:187], v118 offset:18432
	ds_read_b128 v[188:191], v118 offset:19456
	ds_read_b128 v[198:201], v118 offset:20480
	ds_read_b128 v[202:205], v118 offset:21504
	ds_read_b128 v[206:209], v118 offset:22528
	ds_read_b128 v[210:213], v118 offset:23552
	global_load_lds_dwordx4 v[214:215], off
	s_mov_b32 m0, s11
	s_addc_u32 s35, s35, s83
	global_load_lds_dwordx4 v[216:217], off
	v_lshl_add_u64 v[218:219], s[34:35], 0, v[2:3]
	s_mov_b32 m0, s12
	v_lshl_add_u64 v[220:221], s[34:35], 0, v[104:105]
	global_load_lds_dwordx4 v[218:219], off
	s_mov_b32 m0, s13
	v_lshl_add_u64 v[222:223], s[4:5], 0, v[100:101]
	global_load_lds_dwordx4 v[220:221], off
	s_mov_b32 m0, s16
	v_lshl_add_u64 v[224:225], s[4:5], 0, v[102:103]
	global_load_lds_dwordx4 v[222:223], off
	s_mov_b32 m0, s17
	s_nop 0
	global_load_lds_dwordx4 v[224:225], off
	s_waitcnt vmcnt(24)
	s_cmp_lg_u32 s49, 0
	s_cbranch_scc1 .Lpg8f4
	s_waitcnt vmcnt(8)
.Lpg8f4:
	s_waitcnt lgkmcnt(0)
	s_barrier
	s_waitcnt lgkmcnt(0)
	v_mfma_f32_16x16x32_bf16 v[64:67], v[120:123], v[176:179], v[64:67]
	v_mfma_f32_16x16x32_bf16 v[60:63], v[152:155], v[176:179], v[60:63]
	v_mfma_f32_16x16x32_bf16 v[48:51], v[120:123], v[184:187], v[48:51]
	v_mfma_f32_16x16x32_bf16 v[44:47], v[152:155], v[184:187], v[44:47]
	v_mfma_f32_16x16x32_bf16 v[32:35], v[120:123], v[198:201], v[32:35]
	v_mfma_f32_16x16x32_bf16 v[28:31], v[152:155], v[198:201], v[28:31]
	v_mfma_f32_16x16x32_bf16 v[16:19], v[120:123], v[206:209], v[16:19]
	v_mfma_f32_16x16x32_bf16 v[12:15], v[152:155], v[206:209], v[12:15]
	v_mfma_f32_16x16x32_bf16 v[64:67], v[148:151], v[180:183], v[64:67]
	v_mfma_f32_16x16x32_bf16 v[60:63], v[156:159], v[180:183], v[60:63]
	v_mfma_f32_16x16x32_bf16 v[48:51], v[148:151], v[188:191], v[48:51]
	v_mfma_f32_16x16x32_bf16 v[44:47], v[156:159], v[188:191], v[44:47]
	v_mfma_f32_16x16x32_bf16 v[32:35], v[148:151], v[202:205], v[32:35]
	v_mfma_f32_16x16x32_bf16 v[28:31], v[156:159], v[202:205], v[28:31]
	v_mfma_f32_16x16x32_bf16 v[16:19], v[148:151], v[210:213], v[16:19]
	v_mfma_f32_16x16x32_bf16 v[12:15], v[156:159], v[210:213], v[12:15]
	v_mfma_f32_16x16x32_bf16 v[56:59], v[160:163], v[176:179], v[56:59]
	v_mfma_f32_16x16x32_bf16 v[52:55], v[168:171], v[176:179], v[52:55]
	v_mfma_f32_16x16x32_bf16 v[40:43], v[160:163], v[184:187], v[40:43]
	v_mfma_f32_16x16x32_bf16 v[36:39], v[168:171], v[184:187], v[36:39]
	v_mfma_f32_16x16x32_bf16 v[24:27], v[160:163], v[198:201], v[24:27]
	v_mfma_f32_16x16x32_bf16 v[20:23], v[168:171], v[198:201], v[20:23]
	v_mfma_f32_16x16x32_bf16 v[8:11], v[160:163], v[206:209], v[8:11]
	v_mfma_f32_16x16x32_bf16 v[4:7], v[168:171], v[206:209], v[4:7]
	v_mfma_f32_16x16x32_bf16 v[56:59], v[164:167], v[180:183], v[56:59]
	v_mfma_f32_16x16x32_bf16 v[52:55], v[172:175], v[180:183], v[52:55]
	v_mfma_f32_16x16x32_bf16 v[40:43], v[164:167], v[188:191], v[40:43]
	v_mfma_f32_16x16x32_bf16 v[36:39], v[172:175], v[188:191], v[36:39]
	v_mfma_f32_16x16x32_bf16 v[24:27], v[164:167], v[202:205], v[24:27]
	v_mfma_f32_16x16x32_bf16 v[20:23], v[172:175], v[202:205], v[20:23]
	v_mfma_f32_16x16x32_bf16 v[8:11], v[164:167], v[210:213], v[8:11]
	v_mfma_f32_16x16x32_bf16 v[4:7], v[172:175], v[210:213], v[4:7]
	s_barrier
	v_add_u32_e32 v119, s68, v117
	ds_read_b128 v[120:123], v119
	ds_read_b128 v[148:151], v119 offset:1024
	ds_read_b128 v[152:155], v119 offset:2048
	ds_read_b128 v[156:159], v119 offset:3072
	v_add_u32_e32 v119, s69, v117
	ds_read_b128 v[160:163], v119
	ds_read_b128 v[164:167], v119 offset:1024
	ds_read_b128 v[168:171], v119 offset:2048
	ds_read_b128 v[172:175], v119 offset:3072
	s_add_u32 s4, s4, s82
	s_addc_u32 s5, s5, s83
	s_mov_b32 m0, s18
	v_lshl_add_u64 v[226:227], s[4:5], 0, v[100:101]
	ds_read_b128 v[176:179], v118 offset:32768
	ds_read_b128 v[180:183], v118 offset:33792
	ds_read_b128 v[184:187], v118 offset:34816
	ds_read_b128 v[188:191], v118 offset:35840
	ds_read_b128 v[198:201], v118 offset:36864
	ds_read_b128 v[202:205], v118 offset:37888
	ds_read_b128 v[206:209], v118 offset:38912
	ds_read_b128 v[210:213], v118 offset:39936
	global_load_lds_dwordx4 v[226:227], off
	v_lshl_add_u64 v[228:229], s[4:5], 0, v[102:103]
	s_mov_b32 m0, s19
	s_nop 0
	global_load_lds_dwordx4 v[228:229], off
	s_waitcnt vmcnt(24)
	s_cmp_lg_u32 s49, 0
	s_cbranch_scc1 .Lpg8f5
	s_waitcnt vmcnt(8)
.Lpg8f5:
	s_waitcnt lgkmcnt(0)
	s_barrier
	s_waitcnt lgkmcnt(0)
	v_mfma_f32_16x16x32_bf16 v[144:147], v[120:123], v[176:179], v[144:147]
	v_mfma_f32_16x16x32_bf16 v[140:143], v[152:155], v[176:179], v[140:143]
	v_mfma_f32_16x16x32_bf16 v[128:131], v[120:123], v[184:187], v[128:131]
	v_mfma_f32_16x16x32_bf16 v[124:127], v[152:155], v[184:187], v[124:127]
	v_mfma_f32_16x16x32_bf16 v[96:99], v[120:123], v[198:201], v[96:99]
	v_mfma_f32_16x16x32_bf16 v[92:95], v[152:155], v[198:201], v[92:95]
	v_mfma_f32_16x16x32_bf16 v[80:83], v[120:123], v[206:209], v[80:83]
	v_mfma_f32_16x16x32_bf16 v[76:79], v[152:155], v[206:209], v[76:79]
	v_mfma_f32_16x16x32_bf16 v[144:147], v[148:151], v[180:183], v[144:147]
	v_mfma_f32_16x16x32_bf16 v[140:143], v[156:159], v[180:183], v[140:143]
	v_mfma_f32_16x16x32_bf16 v[128:131], v[148:151], v[188:191], v[128:131]
	v_mfma_f32_16x16x32_bf16 v[124:127], v[156:159], v[188:191], v[124:127]
	v_mfma_f32_16x16x32_bf16 v[96:99], v[148:151], v[202:205], v[96:99]
	v_mfma_f32_16x16x32_bf16 v[92:95], v[156:159], v[202:205], v[92:95]
	v_mfma_f32_16x16x32_bf16 v[80:83], v[148:151], v[210:213], v[80:83]
	v_mfma_f32_16x16x32_bf16 v[76:79], v[156:159], v[210:213], v[76:79]
	v_mfma_f32_16x16x32_bf16 v[136:139], v[160:163], v[176:179], v[136:139]
	v_mfma_f32_16x16x32_bf16 v[132:135], v[168:171], v[176:179], v[132:135]
	v_mfma_f32_16x16x32_bf16 v[112:115], v[160:163], v[184:187], v[112:115]
	v_mfma_f32_16x16x32_bf16 v[108:111], v[168:171], v[184:187], v[108:111]
	v_mfma_f32_16x16x32_bf16 v[88:91], v[160:163], v[198:201], v[88:91]
	v_mfma_f32_16x16x32_bf16 v[84:87], v[168:171], v[198:201], v[84:87]
	v_mfma_f32_16x16x32_bf16 v[72:75], v[160:163], v[206:209], v[72:75]
	v_mfma_f32_16x16x32_bf16 v[68:71], v[168:171], v[206:209], v[68:71]
	v_mfma_f32_16x16x32_bf16 v[136:139], v[164:167], v[180:183], v[136:139]
	v_mfma_f32_16x16x32_bf16 v[132:135], v[172:175], v[180:183], v[132:135]
	v_mfma_f32_16x16x32_bf16 v[112:115], v[164:167], v[188:191], v[112:115]
	v_mfma_f32_16x16x32_bf16 v[108:111], v[172:175], v[188:191], v[108:111]
	v_mfma_f32_16x16x32_bf16 v[88:91], v[164:167], v[202:205], v[88:91]
	v_mfma_f32_16x16x32_bf16 v[84:87], v[172:175], v[202:205], v[84:87]
	v_mfma_f32_16x16x32_bf16 v[72:75], v[164:167], v[210:213], v[72:75]
	v_mfma_f32_16x16x32_bf16 v[68:71], v[172:175], v[210:213], v[68:71]
	s_barrier
	s_mov_b32 m0, s20
	v_lshl_add_u64 v[214:215], v[214:215], 0, s[86:87]
	ds_read_b128 v[176:179], v118 offset:49152
	ds_read_b128 v[180:183], v118 offset:50176
	ds_read_b128 v[184:187], v118 offset:51200
	ds_read_b128 v[188:191], v118 offset:52224
	ds_read_b128 v[198:201], v118 offset:53248
	ds_read_b128 v[202:205], v118 offset:54272
	ds_read_b128 v[206:209], v118 offset:55296
	ds_read_b128 v[210:213], v118 offset:56320
	global_load_lds_dwordx4 v[214:215], off
	v_lshl_add_u64 v[214:215], v[216:217], 0, s[86:87]
	s_mov_b32 m0, s21
	s_nop 0
	global_load_lds_dwordx4 v[214:215], off
	v_lshl_add_u64 v[214:215], v[218:219], 0, s[86:87]
	s_mov_b32 m0, s24
	s_nop 0
	global_load_lds_dwordx4 v[214:215], off
	v_lshl_add_u64 v[214:215], v[220:221], 0, s[86:87]
	s_mov_b32 m0, s25
	s_nop 0
	global_load_lds_dwordx4 v[214:215], off
	v_lshl_add_u64 v[214:215], v[222:223], 0, s[86:87]
	s_mov_b32 m0, s22
	s_nop 0
	global_load_lds_dwordx4 v[214:215], off
	v_lshl_add_u64 v[214:215], v[224:225], 0, s[86:87]
	s_mov_b32 m0, s23
	s_nop 0
	global_load_lds_dwordx4 v[214:215], off
	s_waitcnt vmcnt(8)
	s_waitcnt lgkmcnt(0)
	s_barrier
	s_waitcnt lgkmcnt(0)
	v_mfma_f32_16x16x32_bf16 v[64:67], v[120:123], v[176:179], v[64:67]
	v_mfma_f32_16x16x32_bf16 v[60:63], v[152:155], v[176:179], v[60:63]
	v_mfma_f32_16x16x32_bf16 v[48:51], v[120:123], v[184:187], v[48:51]
	v_mfma_f32_16x16x32_bf16 v[44:47], v[152:155], v[184:187], v[44:47]
	v_mfma_f32_16x16x32_bf16 v[32:35], v[120:123], v[198:201], v[32:35]
	v_mfma_f32_16x16x32_bf16 v[28:31], v[152:155], v[198:201], v[28:31]
	v_mfma_f32_16x16x32_bf16 v[16:19], v[120:123], v[206:209], v[16:19]
	v_mfma_f32_16x16x32_bf16 v[12:15], v[152:155], v[206:209], v[12:15]
	v_mfma_f32_16x16x32_bf16 v[64:67], v[148:151], v[180:183], v[64:67]
	v_mfma_f32_16x16x32_bf16 v[60:63], v[156:159], v[180:183], v[60:63]
	v_mfma_f32_16x16x32_bf16 v[48:51], v[148:151], v[188:191], v[48:51]
	v_mfma_f32_16x16x32_bf16 v[44:47], v[156:159], v[188:191], v[44:47]
	v_mfma_f32_16x16x32_bf16 v[32:35], v[148:151], v[202:205], v[32:35]
	v_mfma_f32_16x16x32_bf16 v[28:31], v[156:159], v[202:205], v[28:31]
	v_mfma_f32_16x16x32_bf16 v[16:19], v[148:151], v[210:213], v[16:19]
	v_mfma_f32_16x16x32_bf16 v[12:15], v[156:159], v[210:213], v[12:15]
	v_mfma_f32_16x16x32_bf16 v[56:59], v[160:163], v[176:179], v[56:59]
	v_mfma_f32_16x16x32_bf16 v[52:55], v[168:171], v[176:179], v[52:55]
	v_mfma_f32_16x16x32_bf16 v[40:43], v[160:163], v[184:187], v[40:43]
	v_mfma_f32_16x16x32_bf16 v[36:39], v[168:171], v[184:187], v[36:39]
	v_mfma_f32_16x16x32_bf16 v[24:27], v[160:163], v[198:201], v[24:27]
	v_mfma_f32_16x16x32_bf16 v[20:23], v[168:171], v[198:201], v[20:23]
	v_mfma_f32_16x16x32_bf16 v[8:11], v[160:163], v[206:209], v[8:11]
	v_mfma_f32_16x16x32_bf16 v[4:7], v[168:171], v[206:209], v[4:7]
	v_mfma_f32_16x16x32_bf16 v[56:59], v[164:167], v[180:183], v[56:59]
	v_mfma_f32_16x16x32_bf16 v[52:55], v[172:175], v[180:183], v[52:55]
	v_mfma_f32_16x16x32_bf16 v[40:43], v[164:167], v[188:191], v[40:43]
	v_mfma_f32_16x16x32_bf16 v[36:39], v[172:175], v[188:191], v[36:39]
	v_mfma_f32_16x16x32_bf16 v[24:27], v[164:167], v[202:205], v[24:27]
	v_mfma_f32_16x16x32_bf16 v[20:23], v[172:175], v[202:205], v[20:23]
	v_mfma_f32_16x16x32_bf16 v[8:11], v[164:167], v[210:213], v[8:11]
	v_mfma_f32_16x16x32_bf16 v[4:7], v[172:175], v[210:213], v[4:7]
	s_barrier
	s_mov_b32 m0, s26
	v_lshl_add_u64 v[120:121], v[226:227], 0, s[86:87]
	global_load_lds_dwordx4 v[120:121], off
	v_lshl_add_u64 v[120:121], v[228:229], 0, s[86:87]
	s_mov_b32 m0, s27
	s_nop 0
	global_load_lds_dwordx4 v[120:121], off
	s_add_u32 s28, s28, 0x100
	s_addc_u32 s29, s29, 0
	s_add_u32 s30, s30, 0x100
	s_addc_u32 s31, s31, 0
	s_cmp_ge_i32 s33, s46
	s_mov_b32 s4, s33
	s_cbranch_scc0 .LBB0_684

.Lpg8f6:
	s_waitcnt lgkmcnt(0)
	s_barrier
	s_waitcnt lgkmcnt(0)
	v_mfma_f32_16x16x32_bf16 v[130:133], v[146:149], v[178:181], v[130:133]
	v_mfma_f32_16x16x32_bf16 v[126:129], v[154:157], v[178:181], v[126:129]
	v_mfma_f32_16x16x32_bf16 v[122:125], v[146:149], v[186:189], v[122:125]
	v_mfma_f32_16x16x32_bf16 v[118:121], v[154:157], v[186:189], v[118:121]
	v_mfma_f32_16x16x32_bf16 v[114:117], v[146:149], v[202:205], v[114:117]
	v_mfma_f32_16x16x32_bf16 v[110:113], v[154:157], v[202:205], v[110:113]
	v_mfma_f32_16x16x32_bf16 v[106:109], v[146:149], v[210:213], v[106:109]
	v_mfma_f32_16x16x32_bf16 v[102:105], v[154:157], v[210:213], v[102:105]
	v_mfma_f32_16x16x32_bf16 v[130:133], v[150:153], v[182:185], v[130:133]
	v_mfma_f32_16x16x32_bf16 v[126:129], v[158:161], v[182:185], v[126:129]
	v_mfma_f32_16x16x32_bf16 v[122:125], v[150:153], v[198:201], v[122:125]
	v_mfma_f32_16x16x32_bf16 v[118:121], v[158:161], v[198:201], v[118:121]
	v_mfma_f32_16x16x32_bf16 v[114:117], v[150:153], v[206:209], v[114:117]
	v_mfma_f32_16x16x32_bf16 v[110:113], v[158:161], v[206:209], v[110:113]
	v_mfma_f32_16x16x32_bf16 v[106:109], v[150:153], v[214:217], v[106:109]
	v_mfma_f32_16x16x32_bf16 v[102:105], v[158:161], v[214:217], v[102:105]
	v_mfma_f32_16x16x32_bf16 v[98:101], v[162:165], v[178:181], v[98:101]
	v_mfma_f32_16x16x32_bf16 v[94:97], v[170:173], v[178:181], v[94:97]
	v_mfma_f32_16x16x32_bf16 v[90:93], v[162:165], v[186:189], v[90:93]
	v_mfma_f32_16x16x32_bf16 v[86:89], v[170:173], v[186:189], v[86:89]
	v_mfma_f32_16x16x32_bf16 v[82:85], v[162:165], v[202:205], v[82:85]
	v_mfma_f32_16x16x32_bf16 v[78:81], v[170:173], v[202:205], v[78:81]
	v_mfma_f32_16x16x32_bf16 v[74:77], v[162:165], v[210:213], v[74:77]
	v_mfma_f32_16x16x32_bf16 v[70:73], v[170:173], v[210:213], v[70:73]
	v_mfma_f32_16x16x32_bf16 v[98:101], v[166:169], v[182:185], v[98:101]
	v_mfma_f32_16x16x32_bf16 v[94:97], v[174:177], v[182:185], v[94:97]
	v_mfma_f32_16x16x32_bf16 v[90:93], v[166:169], v[198:201], v[90:93]
	v_mfma_f32_16x16x32_bf16 v[86:89], v[174:177], v[198:201], v[86:89]
	v_mfma_f32_16x16x32_bf16 v[82:85], v[166:169], v[206:209], v[82:85]
	v_mfma_f32_16x16x32_bf16 v[78:81], v[174:177], v[206:209], v[78:81]
	v_mfma_f32_16x16x32_bf16 v[74:77], v[166:169], v[214:217], v[74:77]
	v_mfma_f32_16x16x32_bf16 v[70:73], v[174:177], v[214:217], v[70:73]
	s_barrier
	s_mov_b32 m0, s54
	v_lshl_add_u64 v[190:191], s[40:41], 0, v[138:139]
	v_lshl_add_u64 v[218:219], s[40:41], 0, v[134:135]
	s_add_u32 s40, s40, s14
	ds_read_b128 v[178:181], v227 offset:16384
	ds_read_b128 v[182:185], v227 offset:17408
	ds_read_b128 v[186:189], v227 offset:18432
	ds_read_b128 v[198:201], v227 offset:19456
	ds_read_b128 v[202:205], v227 offset:20480
	ds_read_b128 v[206:209], v227 offset:21504
	ds_read_b128 v[210:213], v227 offset:22528
	ds_read_b128 v[214:217], v227 offset:23552
	global_load_lds_dwordx4 v[190:191], off
	s_mov_b32 m0, s55
	s_addc_u32 s41, s41, s15
	global_load_lds_dwordx4 v[218:219], off
	v_lshl_add_u64 v[220:221], s[40:41], 0, v[138:139]
	s_mov_b32 m0, s57
	v_lshl_add_u64 v[222:223], s[40:41], 0, v[134:135]
	global_load_lds_dwordx4 v[220:221], off
	s_mov_b32 m0, s58
	v_lshl_add_u64 v[224:225], s[38:39], 0, v[140:141]
	global_load_lds_dwordx4 v[222:223], off
	s_mov_b32 m0, s59
	v_lshl_add_u64 v[228:229], s[38:39], 0, v[136:137]
	global_load_lds_dwordx4 v[224:225], off
	s_mov_b32 m0, s60
	s_nop 0
	global_load_lds_dwordx4 v[228:229], off
	s_waitcnt vmcnt(8)
	s_cmp_lg_u32 s42, 0
	s_cbranch_scc1 .Lpg8f7
	s_waitcnt vmcnt(8)
.Lpg8f7:
	s_waitcnt lgkmcnt(0)
	s_barrier
	s_waitcnt lgkmcnt(0)
	v_mfma_f32_16x16x32_bf16 v[66:69], v[146:149], v[178:181], v[66:69]
	v_mfma_f32_16x16x32_bf16 v[62:65], v[154:157], v[178:181], v[62:65]
	v_mfma_f32_16x16x32_bf16 v[58:61], v[146:149], v[186:189], v[58:61]
	v_mfma_f32_16x16x32_bf16 v[54:57], v[154:157], v[186:189], v[54:57]
	v_mfma_f32_16x16x32_bf16 v[50:53], v[146:149], v[202:205], v[50:53]
	v_mfma_f32_16x16x32_bf16 v[46:49], v[154:157], v[202:205], v[46:49]
	v_mfma_f32_16x16x32_bf16 v[42:45], v[146:149], v[210:213], v[42:45]
	v_mfma_f32_16x16x32_bf16 v[38:41], v[154:157], v[210:213], v[38:41]
	v_mfma_f32_16x16x32_bf16 v[66:69], v[150:153], v[182:185], v[66:69]
	v_mfma_f32_16x16x32_bf16 v[62:65], v[158:161], v[182:185], v[62:65]
	v_mfma_f32_16x16x32_bf16 v[58:61], v[150:153], v[198:201], v[58:61]
	v_mfma_f32_16x16x32_bf16 v[54:57], v[158:161], v[198:201], v[54:57]
	v_mfma_f32_16x16x32_bf16 v[50:53], v[150:153], v[206:209], v[50:53]
	v_mfma_f32_16x16x32_bf16 v[46:49], v[158:161], v[206:209], v[46:49]
	v_mfma_f32_16x16x32_bf16 v[42:45], v[150:153], v[214:217], v[42:45]
	v_mfma_f32_16x16x32_bf16 v[38:41], v[158:161], v[214:217], v[38:41]
	v_mfma_f32_16x16x32_bf16 v[34:37], v[162:165], v[178:181], v[34:37]
	v_mfma_f32_16x16x32_bf16 v[30:33], v[170:173], v[178:181], v[30:33]
	v_mfma_f32_16x16x32_bf16 v[26:29], v[162:165], v[186:189], v[26:29]
	v_mfma_f32_16x16x32_bf16 v[22:25], v[170:173], v[186:189], v[22:25]
	v_mfma_f32_16x16x32_bf16 v[18:21], v[162:165], v[202:205], v[18:21]
	v_mfma_f32_16x16x32_bf16 v[14:17], v[170:173], v[202:205], v[14:17]
	v_mfma_f32_16x16x32_bf16 v[10:13], v[162:165], v[210:213], v[10:13]
	v_mfma_f32_16x16x32_bf16 v[4:7], v[170:173], v[210:213], v[6:9]
	v_mfma_f32_16x16x32_bf16 v[34:37], v[166:169], v[182:185], v[34:37]
	v_mfma_f32_16x16x32_bf16 v[30:33], v[174:177], v[182:185], v[30:33]
	v_mfma_f32_16x16x32_bf16 v[26:29], v[166:169], v[198:201], v[26:29]
	v_mfma_f32_16x16x32_bf16 v[22:25], v[174:177], v[198:201], v[22:25]
	v_mfma_f32_16x16x32_bf16 v[18:21], v[166:169], v[206:209], v[18:21]
	v_mfma_f32_16x16x32_bf16 v[14:17], v[174:177], v[206:209], v[14:17]
	v_mfma_f32_16x16x32_bf16 v[10:13], v[166:169], v[214:217], v[10:13]
	v_mfma_f32_16x16x32_bf16 v[4:7], v[174:177], v[214:217], v[4:7]
	s_barrier
	v_add_u32_e32 v2, s66, v226
	ds_read_b128 v[146:149], v2
	ds_read_b128 v[150:153], v2 offset:1024
	ds_read_b128 v[154:157], v2 offset:2048
	ds_read_b128 v[158:161], v2 offset:3072
	v_add_u32_e32 v2, s71, v226
	ds_read_b128 v[162:165], v2
	ds_read_b128 v[166:169], v2 offset:1024
	ds_read_b128 v[170:173], v2 offset:2048
	ds_read_b128 v[174:177], v2 offset:3072
	s_add_u32 s38, s38, s14
	s_addc_u32 s39, s39, s15
	s_mov_b32 m0, s61
	v_lshl_add_u64 v[230:231], s[38:39], 0, v[140:141]
	ds_read_b128 v[178:181], v227 offset:32768
	ds_read_b128 v[182:185], v227 offset:33792
	ds_read_b128 v[186:189], v227 offset:34816
	ds_read_b128 v[198:201], v227 offset:35840
	ds_read_b128 v[202:205], v227 offset:36864
	ds_read_b128 v[206:209], v227 offset:37888
	ds_read_b128 v[210:213], v227 offset:38912
	ds_read_b128 v[214:217], v227 offset:39936
	global_load_lds_dwordx4 v[230:231], off
	v_lshl_add_u64 v[236:237], s[38:39], 0, v[136:137]
	s_mov_b32 m0, s62
	s_nop 0
	global_load_lds_dwordx4 v[236:237], off
	s_waitcnt vmcnt(8)
	s_cmp_lg_u32 s42, 0
	s_cbranch_scc1 .Lpg8f8
	s_waitcnt vmcnt(8)
.Lpg8f8:
	s_waitcnt lgkmcnt(0)
	s_barrier
	s_waitcnt lgkmcnt(0)
	v_mfma_f32_16x16x32_bf16 v[130:133], v[146:149], v[178:181], v[130:133]
	v_mfma_f32_16x16x32_bf16 v[126:129], v[154:157], v[178:181], v[126:129]
	v_mfma_f32_16x16x32_bf16 v[122:125], v[146:149], v[186:189], v[122:125]
	v_mfma_f32_16x16x32_bf16 v[118:121], v[154:157], v[186:189], v[118:121]
	v_mfma_f32_16x16x32_bf16 v[114:117], v[146:149], v[202:205], v[114:117]
	v_mfma_f32_16x16x32_bf16 v[110:113], v[154:157], v[202:205], v[110:113]
	v_mfma_f32_16x16x32_bf16 v[106:109], v[146:149], v[210:213], v[106:109]
	v_mfma_f32_16x16x32_bf16 v[102:105], v[154:157], v[210:213], v[102:105]
	v_mfma_f32_16x16x32_bf16 v[130:133], v[150:153], v[182:185], v[130:133]
	v_mfma_f32_16x16x32_bf16 v[126:129], v[158:161], v[182:185], v[126:129]
	v_mfma_f32_16x16x32_bf16 v[122:125], v[150:153], v[198:201], v[122:125]
	v_mfma_f32_16x16x32_bf16 v[118:121], v[158:161], v[198:201], v[118:121]
	v_mfma_f32_16x16x32_bf16 v[114:117], v[150:153], v[206:209], v[114:117]
	v_mfma_f32_16x16x32_bf16 v[110:113], v[158:161], v[206:209], v[110:113]
	v_mfma_f32_16x16x32_bf16 v[106:109], v[150:153], v[214:217], v[106:109]
	v_mfma_f32_16x16x32_bf16 v[102:105], v[158:161], v[214:217], v[102:105]
	v_mfma_f32_16x16x32_bf16 v[98:101], v[162:165], v[178:181], v[98:101]
	v_mfma_f32_16x16x32_bf16 v[94:97], v[170:173], v[178:181], v[94:97]
	v_mfma_f32_16x16x32_bf16 v[90:93], v[162:165], v[186:189], v[90:93]
	v_mfma_f32_16x16x32_bf16 v[86:89], v[170:173], v[186:189], v[86:89]
	v_mfma_f32_16x16x32_bf16 v[82:85], v[162:165], v[202:205], v[82:85]
	v_mfma_f32_16x16x32_bf16 v[78:81], v[170:173], v[202:205], v[78:81]
	v_mfma_f32_16x16x32_bf16 v[74:77], v[162:165], v[210:213], v[74:77]
	v_mfma_f32_16x16x32_bf16 v[70:73], v[170:173], v[210:213], v[70:73]
	v_mfma_f32_16x16x32_bf16 v[98:101], v[166:169], v[182:185], v[98:101]
	v_mfma_f32_16x16x32_bf16 v[94:97], v[174:177], v[182:185], v[94:97]
	v_mfma_f32_16x16x32_bf16 v[90:93], v[166:169], v[198:201], v[90:93]
	v_mfma_f32_16x16x32_bf16 v[86:89], v[174:177], v[198:201], v[86:89]
	v_mfma_f32_16x16x32_bf16 v[82:85], v[166:169], v[206:209], v[82:85]
	v_mfma_f32_16x16x32_bf16 v[78:81], v[174:177], v[206:209], v[78:81]
	v_mfma_f32_16x16x32_bf16 v[74:77], v[166:169], v[214:217], v[74:77]
	v_mfma_f32_16x16x32_bf16 v[70:73], v[174:177], v[214:217], v[70:73]
	s_barrier
	s_mov_b32 m0, s67
	v_lshl_add_u64 v[8:9], v[190:191], 0, s[86:87]
	ds_read_b128 v[178:181], v227 offset:49152
	ds_read_b128 v[182:185], v227 offset:50176
	ds_read_b128 v[186:189], v227 offset:51200
	ds_read_b128 v[198:201], v227 offset:52224
	ds_read_b128 v[202:205], v227 offset:53248
	ds_read_b128 v[206:209], v227 offset:54272
	ds_read_b128 v[210:213], v227 offset:55296
	ds_read_b128 v[214:217], v227 offset:56320
	global_load_lds_dwordx4 v[8:9], off
	v_lshl_add_u64 v[8:9], v[218:219], 0, s[86:87]
	s_mov_b32 m0, s68
	s_nop 0
	global_load_lds_dwordx4 v[8:9], off
	v_lshl_add_u64 v[8:9], v[220:221], 0, s[86:87]
	s_mov_b32 m0, s72
	s_nop 0
	global_load_lds_dwordx4 v[8:9], off
	v_lshl_add_u64 v[8:9], v[222:223], 0, s[86:87]
	s_mov_b32 m0, s73
	s_nop 0
	global_load_lds_dwordx4 v[8:9], off
	v_lshl_add_u64 v[8:9], v[224:225], 0, s[86:87]
	s_mov_b32 m0, s69
	s_nop 0
	global_load_lds_dwordx4 v[8:9], off
	v_lshl_add_u64 v[8:9], v[228:229], 0, s[86:87]
	s_mov_b32 m0, s70
	s_nop 0
	global_load_lds_dwordx4 v[8:9], off
	s_waitcnt vmcnt(8)
	s_waitcnt lgkmcnt(0)
	s_barrier
	s_waitcnt lgkmcnt(0)
	v_mfma_f32_16x16x32_bf16 v[66:69], v[146:149], v[178:181], v[66:69]
	v_mfma_f32_16x16x32_bf16 v[62:65], v[154:157], v[178:181], v[62:65]
	v_mfma_f32_16x16x32_bf16 v[58:61], v[146:149], v[186:189], v[58:61]
	v_mfma_f32_16x16x32_bf16 v[54:57], v[154:157], v[186:189], v[54:57]
	v_mfma_f32_16x16x32_bf16 v[50:53], v[146:149], v[202:205], v[50:53]
	v_mfma_f32_16x16x32_bf16 v[46:49], v[154:157], v[202:205], v[46:49]
	v_mfma_f32_16x16x32_bf16 v[42:45], v[146:149], v[210:213], v[42:45]
	v_mfma_f32_16x16x32_bf16 v[38:41], v[154:157], v[210:213], v[38:41]
	v_mfma_f32_16x16x32_bf16 v[66:69], v[150:153], v[182:185], v[66:69]
	v_mfma_f32_16x16x32_bf16 v[62:65], v[158:161], v[182:185], v[62:65]
	v_mfma_f32_16x16x32_bf16 v[58:61], v[150:153], v[198:201], v[58:61]
	v_mfma_f32_16x16x32_bf16 v[54:57], v[158:161], v[198:201], v[54:57]
	v_mfma_f32_16x16x32_bf16 v[50:53], v[150:153], v[206:209], v[50:53]
	v_mfma_f32_16x16x32_bf16 v[46:49], v[158:161], v[206:209], v[46:49]
	v_mfma_f32_16x16x32_bf16 v[42:45], v[150:153], v[214:217], v[42:45]
	v_mfma_f32_16x16x32_bf16 v[38:41], v[158:161], v[214:217], v[38:41]
	v_mfma_f32_16x16x32_bf16 v[34:37], v[162:165], v[178:181], v[34:37]
	v_mfma_f32_16x16x32_bf16 v[30:33], v[170:173], v[178:181], v[30:33]
	v_mfma_f32_16x16x32_bf16 v[26:29], v[162:165], v[186:189], v[26:29]
	v_mfma_f32_16x16x32_bf16 v[22:25], v[170:173], v[186:189], v[22:25]
	v_mfma_f32_16x16x32_bf16 v[18:21], v[162:165], v[202:205], v[18:21]
	v_mfma_f32_16x16x32_bf16 v[14:17], v[170:173], v[202:205], v[14:17]
	v_mfma_f32_16x16x32_bf16 v[8:11], v[162:165], v[210:213], v[10:13]
	v_mfma_f32_16x16x32_bf16 v[4:7], v[170:173], v[210:213], v[4:7]
	v_mfma_f32_16x16x32_bf16 v[34:37], v[166:169], v[182:185], v[34:37]
	v_mfma_f32_16x16x32_bf16 v[30:33], v[174:177], v[182:185], v[30:33]
	v_mfma_f32_16x16x32_bf16 v[26:29], v[166:169], v[198:201], v[26:29]
	v_mfma_f32_16x16x32_bf16 v[22:25], v[174:177], v[198:201], v[22:25]
	v_mfma_f32_16x16x32_bf16 v[18:21], v[166:169], v[206:209], v[18:21]
	v_mfma_f32_16x16x32_bf16 v[14:17], v[174:177], v[206:209], v[14:17]
	v_mfma_f32_16x16x32_bf16 v[10:13], v[166:169], v[214:217], v[8:11]
	v_mfma_f32_16x16x32_bf16 v[6:9], v[174:177], v[214:217], v[4:7]
	s_barrier
	s_mov_b32 m0, s76
	v_lshl_add_u64 v[4:5], v[230:231], 0, s[86:87]
	global_load_lds_dwordx4 v[4:5], off
	v_lshl_add_u64 v[4:5], v[236:237], 0, s[86:87]
	s_mov_b32 m0, s77
	s_nop 0
	global_load_lds_dwordx4 v[4:5], off
	s_cmp_ge_i32 s48, s78
	s_cbranch_scc1 .LBB0_2037
	s_mov_b32 s91, s48
	s_branch .LBB0_2019

.Lpg8f9:
	s_waitcnt lgkmcnt(0)
	s_barrier
	s_waitcnt lgkmcnt(0)
	v_mfma_f32_16x16x32_bf16 v[132:135], v[124:127], v[164:167], v[132:135]
	v_mfma_f32_16x16x32_bf16 v[128:131], v[140:143], v[164:167], v[128:131]
	v_mfma_f32_16x16x32_bf16 v[112:115], v[124:127], v[172:175], v[112:115]
	v_mfma_f32_16x16x32_bf16 v[108:111], v[140:143], v[172:175], v[108:111]
	v_mfma_f32_16x16x32_bf16 v[96:99], v[124:127], v[180:183], v[96:99]
	v_mfma_f32_16x16x32_bf16 v[92:95], v[140:143], v[180:183], v[92:95]
	v_mfma_f32_16x16x32_bf16 v[80:83], v[124:127], v[200:203], v[80:83]
	v_mfma_f32_16x16x32_bf16 v[76:79], v[140:143], v[200:203], v[76:79]
	v_mfma_f32_16x16x32_bf16 v[132:135], v[136:139], v[168:171], v[132:135]
	v_mfma_f32_16x16x32_bf16 v[128:131], v[144:147], v[168:171], v[128:131]
	v_mfma_f32_16x16x32_bf16 v[112:115], v[136:139], v[176:179], v[112:115]
	v_mfma_f32_16x16x32_bf16 v[108:111], v[144:147], v[176:179], v[108:111]
	v_mfma_f32_16x16x32_bf16 v[96:99], v[136:139], v[184:187], v[96:99]
	v_mfma_f32_16x16x32_bf16 v[92:95], v[144:147], v[184:187], v[92:95]
	v_mfma_f32_16x16x32_bf16 v[80:83], v[136:139], v[204:207], v[80:83]
	v_mfma_f32_16x16x32_bf16 v[76:79], v[144:147], v[204:207], v[76:79]
	v_mfma_f32_16x16x32_bf16 v[120:123], v[148:151], v[164:167], v[120:123]
	v_mfma_f32_16x16x32_bf16 v[116:119], v[156:159], v[164:167], v[116:119]
	v_mfma_f32_16x16x32_bf16 v[104:107], v[148:151], v[172:175], v[104:107]
	v_mfma_f32_16x16x32_bf16 v[100:103], v[156:159], v[172:175], v[100:103]
	v_mfma_f32_16x16x32_bf16 v[88:91], v[148:151], v[180:183], v[88:91]
	v_mfma_f32_16x16x32_bf16 v[84:87], v[156:159], v[180:183], v[84:87]
	v_mfma_f32_16x16x32_bf16 v[72:75], v[148:151], v[200:203], v[72:75]
	v_mfma_f32_16x16x32_bf16 v[68:71], v[156:159], v[200:203], v[68:71]
	v_mfma_f32_16x16x32_bf16 v[120:123], v[152:155], v[168:171], v[120:123]
	v_mfma_f32_16x16x32_bf16 v[116:119], v[160:163], v[168:171], v[116:119]
	v_mfma_f32_16x16x32_bf16 v[104:107], v[152:155], v[176:179], v[104:107]
	v_mfma_f32_16x16x32_bf16 v[100:103], v[160:163], v[176:179], v[100:103]
	v_mfma_f32_16x16x32_bf16 v[88:91], v[152:155], v[184:187], v[88:91]
	v_mfma_f32_16x16x32_bf16 v[84:87], v[160:163], v[184:187], v[84:87]
	v_mfma_f32_16x16x32_bf16 v[72:75], v[152:155], v[204:207], v[72:75]
	v_mfma_f32_16x16x32_bf16 v[68:71], v[160:163], v[204:207], v[68:71]
	s_barrier
	s_mov_b32 m0, s36
	v_lshl_add_u64 v[208:209], s[28:29], 0, v[2:3]
	s_add_u32 s66, s28, 0x40000
	ds_read_b128 v[164:167], v238 offset:16384
	ds_read_b128 v[168:171], v238 offset:17408
	ds_read_b128 v[172:175], v238 offset:18432
	ds_read_b128 v[176:179], v238 offset:19456
	ds_read_b128 v[180:183], v238 offset:20480
	ds_read_b128 v[184:187], v238 offset:21504
	ds_read_b128 v[200:203], v238 offset:22528
	ds_read_b128 v[204:207], v238 offset:23552
	global_load_lds_dwordx4 v[208:209], off
	v_lshl_add_u64 v[210:211], s[28:29], 0, v[188:189]
	s_mov_b32 m0, s37
	s_addc_u32 s67, s29, 0
	global_load_lds_dwordx4 v[210:211], off
	v_lshl_add_u64 v[212:213], s[66:67], 0, v[2:3]
	s_mov_b32 m0, s39
	v_lshl_add_u64 v[214:215], s[26:27], 0, v[190:191]
	global_load_lds_dwordx4 v[212:213], off
	v_lshl_add_u64 v[212:213], s[66:67], 0, v[188:189]
	s_mov_b32 m0, s40
	s_nop 0
	global_load_lds_dwordx4 v[212:213], off
	v_lshl_add_u64 v[212:213], s[26:27], 0, v[198:199]
	s_mov_b32 m0, s41
	s_nop 0
	global_load_lds_dwordx4 v[212:213], off
	s_mov_b32 m0, s42
	s_nop 0
	global_load_lds_dwordx4 v[214:215], off
	s_waitcnt vmcnt(40)
	s_cmp_lg_u32 s63, 0
	s_cbranch_scc1 .Lpg8f10
	s_waitcnt vmcnt(8)
.Lpg8f10:
	s_waitcnt lgkmcnt(0)
	s_barrier
	s_waitcnt lgkmcnt(0)
	v_mfma_f32_16x16x32_bf16 v[64:67], v[124:127], v[164:167], v[64:67]
	v_mfma_f32_16x16x32_bf16 v[60:63], v[140:143], v[164:167], v[60:63]
	v_mfma_f32_16x16x32_bf16 v[48:51], v[124:127], v[172:175], v[48:51]
	v_mfma_f32_16x16x32_bf16 v[44:47], v[140:143], v[172:175], v[44:47]
	v_mfma_f32_16x16x32_bf16 v[32:35], v[124:127], v[180:183], v[32:35]
	v_mfma_f32_16x16x32_bf16 v[28:31], v[140:143], v[180:183], v[28:31]
	v_mfma_f32_16x16x32_bf16 v[16:19], v[124:127], v[200:203], v[16:19]
	v_mfma_f32_16x16x32_bf16 v[12:15], v[140:143], v[200:203], v[12:15]
	v_mfma_f32_16x16x32_bf16 v[64:67], v[136:139], v[168:171], v[64:67]
	v_mfma_f32_16x16x32_bf16 v[60:63], v[144:147], v[168:171], v[60:63]
	v_mfma_f32_16x16x32_bf16 v[48:51], v[136:139], v[176:179], v[48:51]
	v_mfma_f32_16x16x32_bf16 v[44:47], v[144:147], v[176:179], v[44:47]
	v_mfma_f32_16x16x32_bf16 v[32:35], v[136:139], v[184:187], v[32:35]
	v_mfma_f32_16x16x32_bf16 v[28:31], v[144:147], v[184:187], v[28:31]
	v_mfma_f32_16x16x32_bf16 v[16:19], v[136:139], v[204:207], v[16:19]
	v_mfma_f32_16x16x32_bf16 v[12:15], v[144:147], v[204:207], v[12:15]
	v_mfma_f32_16x16x32_bf16 v[56:59], v[148:151], v[164:167], v[56:59]
	v_mfma_f32_16x16x32_bf16 v[52:55], v[156:159], v[164:167], v[52:55]
	v_mfma_f32_16x16x32_bf16 v[40:43], v[148:151], v[172:175], v[40:43]
	v_mfma_f32_16x16x32_bf16 v[36:39], v[156:159], v[172:175], v[36:39]
	v_mfma_f32_16x16x32_bf16 v[24:27], v[148:151], v[180:183], v[24:27]
	v_mfma_f32_16x16x32_bf16 v[20:23], v[156:159], v[180:183], v[20:23]
	v_mfma_f32_16x16x32_bf16 v[8:11], v[148:151], v[200:203], v[8:11]
	v_mfma_f32_16x16x32_bf16 v[4:7], v[156:159], v[200:203], v[4:7]
	v_mfma_f32_16x16x32_bf16 v[56:59], v[152:155], v[168:171], v[56:59]
	v_mfma_f32_16x16x32_bf16 v[52:55], v[160:163], v[168:171], v[52:55]
	v_mfma_f32_16x16x32_bf16 v[40:43], v[152:155], v[176:179], v[40:43]
	v_mfma_f32_16x16x32_bf16 v[36:39], v[160:163], v[176:179], v[36:39]
	v_mfma_f32_16x16x32_bf16 v[24:27], v[152:155], v[184:187], v[24:27]
	v_mfma_f32_16x16x32_bf16 v[20:23], v[160:163], v[184:187], v[20:23]
	v_mfma_f32_16x16x32_bf16 v[8:11], v[152:155], v[204:207], v[8:11]
	v_mfma_f32_16x16x32_bf16 v[4:7], v[160:163], v[204:207], v[4:7]
	s_barrier
	v_add_u32_e32 v144, s46, v235
	v_add_u32_e32 v160, s53, v235
	ds_read_b128 v[124:127], v144
	ds_read_b128 v[136:139], v144 offset:1024
	ds_read_b128 v[140:143], v144 offset:2048
	ds_read_b128 v[144:147], v144 offset:3072
	ds_read_b128 v[148:151], v160
	ds_read_b128 v[152:155], v160 offset:1024
	ds_read_b128 v[156:159], v160 offset:2048
	ds_read_b128 v[160:163], v160 offset:3072
	s_add_u32 s66, s26, 0x40000
	s_addc_u32 s67, s27, 0
	s_mov_b32 m0, s43
	v_lshl_add_u64 v[216:217], s[66:67], 0, v[198:199]
	ds_read_b128 v[164:167], v238 offset:32768
	ds_read_b128 v[168:171], v238 offset:33792
	ds_read_b128 v[172:175], v238 offset:34816
	ds_read_b128 v[176:179], v238 offset:35840
	ds_read_b128 v[180:183], v238 offset:36864
	ds_read_b128 v[184:187], v238 offset:37888
	ds_read_b128 v[200:203], v238 offset:38912
	ds_read_b128 v[204:207], v238 offset:39936
	global_load_lds_dwordx4 v[216:217], off
	v_lshl_add_u64 v[216:217], s[66:67], 0, v[190:191]
	s_mov_b32 m0, s44
	s_nop 0
	global_load_lds_dwordx4 v[216:217], off
	s_waitcnt vmcnt(40)
	s_cmp_lg_u32 s63, 0
	s_cbranch_scc1 .Lpg8f11
	s_waitcnt vmcnt(8)
.Lpg8f11:
	s_waitcnt lgkmcnt(0)
	s_barrier
	s_waitcnt lgkmcnt(0)
	v_mfma_f32_16x16x32_bf16 v[132:135], v[124:127], v[164:167], v[132:135]
	v_mfma_f32_16x16x32_bf16 v[128:131], v[140:143], v[164:167], v[128:131]
	v_mfma_f32_16x16x32_bf16 v[112:115], v[124:127], v[172:175], v[112:115]
	v_mfma_f32_16x16x32_bf16 v[108:111], v[140:143], v[172:175], v[108:111]
	v_mfma_f32_16x16x32_bf16 v[96:99], v[124:127], v[180:183], v[96:99]
	v_mfma_f32_16x16x32_bf16 v[92:95], v[140:143], v[180:183], v[92:95]
	v_mfma_f32_16x16x32_bf16 v[80:83], v[124:127], v[200:203], v[80:83]
	v_mfma_f32_16x16x32_bf16 v[76:79], v[140:143], v[200:203], v[76:79]
	v_mfma_f32_16x16x32_bf16 v[132:135], v[136:139], v[168:171], v[132:135]
	v_mfma_f32_16x16x32_bf16 v[128:131], v[144:147], v[168:171], v[128:131]
	v_mfma_f32_16x16x32_bf16 v[112:115], v[136:139], v[176:179], v[112:115]
	v_mfma_f32_16x16x32_bf16 v[108:111], v[144:147], v[176:179], v[108:111]
	v_mfma_f32_16x16x32_bf16 v[96:99], v[136:139], v[184:187], v[96:99]
	v_mfma_f32_16x16x32_bf16 v[92:95], v[144:147], v[184:187], v[92:95]
	v_mfma_f32_16x16x32_bf16 v[80:83], v[136:139], v[204:207], v[80:83]
	v_mfma_f32_16x16x32_bf16 v[76:79], v[144:147], v[204:207], v[76:79]
	v_mfma_f32_16x16x32_bf16 v[120:123], v[148:151], v[164:167], v[120:123]
	v_mfma_f32_16x16x32_bf16 v[116:119], v[156:159], v[164:167], v[116:119]
	v_mfma_f32_16x16x32_bf16 v[104:107], v[148:151], v[172:175], v[104:107]
	v_mfma_f32_16x16x32_bf16 v[100:103], v[156:159], v[172:175], v[100:103]
	v_mfma_f32_16x16x32_bf16 v[88:91], v[148:151], v[180:183], v[88:91]
	v_mfma_f32_16x16x32_bf16 v[84:87], v[156:159], v[180:183], v[84:87]
	v_mfma_f32_16x16x32_bf16 v[72:75], v[148:151], v[200:203], v[72:75]
	v_mfma_f32_16x16x32_bf16 v[68:71], v[156:159], v[200:203], v[68:71]
	v_mfma_f32_16x16x32_bf16 v[120:123], v[152:155], v[168:171], v[120:123]
	v_mfma_f32_16x16x32_bf16 v[116:119], v[160:163], v[168:171], v[116:119]
	v_mfma_f32_16x16x32_bf16 v[104:107], v[152:155], v[176:179], v[104:107]
	v_mfma_f32_16x16x32_bf16 v[100:103], v[160:163], v[176:179], v[100:103]
	v_mfma_f32_16x16x32_bf16 v[88:91], v[152:155], v[184:187], v[88:91]
	v_mfma_f32_16x16x32_bf16 v[84:87], v[160:163], v[184:187], v[84:87]
	v_mfma_f32_16x16x32_bf16 v[72:75], v[152:155], v[204:207], v[72:75]
	v_mfma_f32_16x16x32_bf16 v[68:71], v[160:163], v[204:207], v[68:71]
	s_barrier
	s_mov_b32 m0, s47
	v_lshl_add_u64 v[208:209], v[208:209], 0, s[86:87]
	s_add_u32 s28, s28, 0x40080
	ds_read_b128 v[164:167], v238 offset:49152
	ds_read_b128 v[168:171], v238 offset:50176
	ds_read_b128 v[172:175], v238 offset:51200
	ds_read_b128 v[176:179], v238 offset:52224
	ds_read_b128 v[180:183], v238 offset:53248
	ds_read_b128 v[184:187], v238 offset:54272
	ds_read_b128 v[200:203], v238 offset:55296
	ds_read_b128 v[204:207], v238 offset:56320
	global_load_lds_dwordx4 v[208:209], off
	v_lshl_add_u64 v[208:209], v[210:211], 0, s[86:87]
	s_mov_b32 m0, s50
	s_addc_u32 s29, s29, 0
	global_load_lds_dwordx4 v[208:209], off
	v_lshl_add_u64 v[208:209], s[28:29], 0, v[2:3]
	s_mov_b32 m0, s54
	s_nop 0
	global_load_lds_dwordx4 v[208:209], off
	v_lshl_add_u64 v[208:209], s[28:29], 0, v[188:189]
	s_mov_b32 m0, s55
	s_nop 0
	global_load_lds_dwordx4 v[208:209], off
	v_lshl_add_u64 v[208:209], v[212:213], 0, s[86:87]
	s_mov_b32 m0, s51
	s_nop 0
	global_load_lds_dwordx4 v[208:209], off
	v_lshl_add_u64 v[208:209], v[214:215], 0, s[86:87]
	s_mov_b32 m0, s52
	s_nop 0
	global_load_lds_dwordx4 v[208:209], off
	s_waitcnt vmcnt(8)
	s_waitcnt lgkmcnt(0)
	s_barrier
	s_waitcnt lgkmcnt(0)
	v_mfma_f32_16x16x32_bf16 v[64:67], v[124:127], v[164:167], v[64:67]
	v_mfma_f32_16x16x32_bf16 v[60:63], v[140:143], v[164:167], v[60:63]
	v_mfma_f32_16x16x32_bf16 v[48:51], v[124:127], v[172:175], v[48:51]
	v_mfma_f32_16x16x32_bf16 v[44:47], v[140:143], v[172:175], v[44:47]
	v_mfma_f32_16x16x32_bf16 v[32:35], v[124:127], v[180:183], v[32:35]
	v_mfma_f32_16x16x32_bf16 v[28:31], v[140:143], v[180:183], v[28:31]
	v_mfma_f32_16x16x32_bf16 v[16:19], v[124:127], v[200:203], v[16:19]
	v_mfma_f32_16x16x32_bf16 v[12:15], v[140:143], v[200:203], v[12:15]
	v_mfma_f32_16x16x32_bf16 v[64:67], v[136:139], v[168:171], v[64:67]
	v_mfma_f32_16x16x32_bf16 v[60:63], v[144:147], v[168:171], v[60:63]
	v_mfma_f32_16x16x32_bf16 v[48:51], v[136:139], v[176:179], v[48:51]
	v_mfma_f32_16x16x32_bf16 v[44:47], v[144:147], v[176:179], v[44:47]
	v_mfma_f32_16x16x32_bf16 v[32:35], v[136:139], v[184:187], v[32:35]
	v_mfma_f32_16x16x32_bf16 v[28:31], v[144:147], v[184:187], v[28:31]
	v_mfma_f32_16x16x32_bf16 v[16:19], v[136:139], v[204:207], v[16:19]
	v_mfma_f32_16x16x32_bf16 v[12:15], v[144:147], v[204:207], v[12:15]
	v_mfma_f32_16x16x32_bf16 v[56:59], v[148:151], v[164:167], v[56:59]
	v_mfma_f32_16x16x32_bf16 v[52:55], v[156:159], v[164:167], v[52:55]
	v_mfma_f32_16x16x32_bf16 v[40:43], v[148:151], v[172:175], v[40:43]
	v_mfma_f32_16x16x32_bf16 v[36:39], v[156:159], v[172:175], v[36:39]
	v_mfma_f32_16x16x32_bf16 v[24:27], v[148:151], v[180:183], v[24:27]
	v_mfma_f32_16x16x32_bf16 v[20:23], v[156:159], v[180:183], v[20:23]
	v_mfma_f32_16x16x32_bf16 v[8:11], v[148:151], v[200:203], v[8:11]
	v_mfma_f32_16x16x32_bf16 v[4:7], v[156:159], v[200:203], v[4:7]
	v_mfma_f32_16x16x32_bf16 v[56:59], v[152:155], v[168:171], v[56:59]
	v_mfma_f32_16x16x32_bf16 v[52:55], v[160:163], v[168:171], v[52:55]
	v_mfma_f32_16x16x32_bf16 v[40:43], v[152:155], v[176:179], v[40:43]
	v_mfma_f32_16x16x32_bf16 v[36:39], v[160:163], v[176:179], v[36:39]
	v_mfma_f32_16x16x32_bf16 v[24:27], v[152:155], v[184:187], v[24:27]
	v_mfma_f32_16x16x32_bf16 v[20:23], v[160:163], v[184:187], v[20:23]
	v_mfma_f32_16x16x32_bf16 v[8:11], v[152:155], v[204:207], v[8:11]
	v_mfma_f32_16x16x32_bf16 v[4:7], v[160:163], v[204:207], v[4:7]
	s_barrier
	s_add_u32 s26, s26, 0x40080
	s_addc_u32 s27, s27, 0
	s_mov_b32 m0, s56
	v_lshl_add_u64 v[124:125], s[26:27], 0, v[198:199]
	global_load_lds_dwordx4 v[124:125], off
	v_lshl_add_u64 v[124:125], s[26:27], 0, v[190:191]
	s_mov_b32 m0, s57
	s_nop 0
	global_load_lds_dwordx4 v[124:125], off
	s_add_i32 s62, s62, 2
	s_add_u32 s19, s19, 0x100
	s_addc_u32 s21, s21, 0
	s_add_u32 s60, s60, 0x100
	s_addc_u32 s61, s61, 0
	s_cmp_gt_u32 s62, 13
	s_cbranch_scc0 .LBB0_2169
	v_mov_b64_e32 v[192:193], 0xff
	v_mov_b64_e32 v[196:197], 0x100
	s_and_b64 vcc, exec, s[16:17]
	s_cbranch_vccz .LBB0_2172
	s_barrier

.Lpg8f12:
	s_waitcnt lgkmcnt(0)
	s_barrier
	s_waitcnt lgkmcnt(0)
	v_mfma_f32_16x16x32_bf16 v[144:147], v[154:157], v[202:205], v[144:147]
	v_mfma_f32_16x16x32_bf16 v[136:139], v[172:175], v[202:205], v[136:139]
	v_mfma_f32_16x16x32_bf16 v[128:131], v[154:157], v[210:213], v[128:131]
	v_mfma_f32_16x16x32_bf16 v[120:123], v[172:175], v[210:213], v[120:123]
	v_mfma_f32_16x16x32_bf16 v[112:115], v[154:157], v[218:221], v[112:115]
	v_mfma_f32_16x16x32_bf16 v[104:107], v[172:175], v[218:221], v[104:107]
	v_mfma_f32_16x16x32_bf16 v[96:99], v[154:157], v[226:229], v[96:99]
	v_mfma_f32_16x16x32_bf16 v[88:91], v[172:175], v[226:229], v[88:91]
	v_mfma_f32_16x16x32_bf16 v[144:147], v[168:171], v[206:209], v[144:147]
	v_mfma_f32_16x16x32_bf16 v[136:139], v[176:179], v[206:209], v[136:139]
	v_mfma_f32_16x16x32_bf16 v[128:131], v[168:171], v[214:217], v[128:131]
	v_mfma_f32_16x16x32_bf16 v[120:123], v[176:179], v[214:217], v[120:123]
	v_mfma_f32_16x16x32_bf16 v[112:115], v[168:171], v[222:225], v[112:115]
	v_mfma_f32_16x16x32_bf16 v[104:107], v[176:179], v[222:225], v[104:107]
	v_mfma_f32_16x16x32_bf16 v[96:99], v[168:171], v[236:239], v[96:99]
	v_mfma_f32_16x16x32_bf16 v[88:91], v[176:179], v[236:239], v[88:91]
	v_mfma_f32_16x16x32_bf16 v[140:143], v[180:183], v[202:205], v[140:143]
	v_mfma_f32_16x16x32_bf16 v[132:135], v[188:191], v[202:205], v[132:135]
	v_mfma_f32_16x16x32_bf16 v[124:127], v[180:183], v[210:213], v[124:127]
	v_mfma_f32_16x16x32_bf16 v[116:119], v[188:191], v[210:213], v[116:119]
	v_mfma_f32_16x16x32_bf16 v[108:111], v[180:183], v[218:221], v[108:111]
	v_mfma_f32_16x16x32_bf16 v[100:103], v[188:191], v[218:221], v[100:103]
	v_mfma_f32_16x16x32_bf16 v[92:95], v[180:183], v[226:229], v[92:95]
	v_mfma_f32_16x16x32_bf16 v[84:87], v[188:191], v[226:229], v[84:87]
	v_mfma_f32_16x16x32_bf16 v[140:143], v[184:187], v[206:209], v[140:143]
	v_mfma_f32_16x16x32_bf16 v[132:135], v[198:201], v[206:209], v[132:135]
	v_mfma_f32_16x16x32_bf16 v[124:127], v[184:187], v[214:217], v[124:127]
	v_mfma_f32_16x16x32_bf16 v[116:119], v[198:201], v[214:217], v[116:119]
	v_mfma_f32_16x16x32_bf16 v[108:111], v[184:187], v[222:225], v[108:111]
	v_mfma_f32_16x16x32_bf16 v[100:103], v[198:201], v[222:225], v[100:103]
	v_mfma_f32_16x16x32_bf16 v[92:95], v[184:187], v[236:239], v[92:95]
	v_mfma_f32_16x16x32_bf16 v[84:87], v[198:201], v[236:239], v[84:87]
	s_barrier
	s_mov_b32 m0, s38
	v_lshl_add_u64 v[158:159], s[30:31], 0, v[2:3]
	s_add_u32 s68, s30, 0x40000
	ds_read_b128 v[202:205], v166 offset:16384
	ds_read_b128 v[206:209], v166 offset:17408
	ds_read_b128 v[210:213], v166 offset:18432
	ds_read_b128 v[214:217], v166 offset:19456
	ds_read_b128 v[218:221], v166 offset:20480
	ds_read_b128 v[222:225], v166 offset:21504
	ds_read_b128 v[226:229], v166 offset:22528
	ds_read_b128 v[236:239], v166 offset:23552
	global_load_lds_dwordx4 v[158:159], off
	v_lshl_add_u64 v[194:195], s[30:31], 0, v[152:153]
	s_mov_b32 m0, s39
	s_addc_u32 s69, s31, 0
	global_load_lds_dwordx4 v[194:195], off
	v_lshl_add_u64 v[230:231], s[68:69], 0, v[2:3]
	s_mov_b32 m0, s41
	v_lshl_add_u64 v[240:241], s[28:29], 0, v[150:151]
	global_load_lds_dwordx4 v[230:231], off
	v_lshl_add_u64 v[230:231], s[68:69], 0, v[152:153]
	s_mov_b32 m0, s43
	s_nop 0
	global_load_lds_dwordx4 v[230:231], off
	v_lshl_add_u64 v[230:231], s[28:29], 0, v[148:149]
	s_mov_b32 m0, s44
	s_nop 0
	global_load_lds_dwordx4 v[230:231], off
	s_mov_b32 m0, s45
	s_nop 0
	global_load_lds_dwordx4 v[240:241], off
	s_waitcnt vmcnt(16)
	s_cmp_lg_u32 s67, 0
	s_cbranch_scc1 .Lpg8f13
	s_waitcnt vmcnt(8)
.Lpg8f13:
	s_waitcnt lgkmcnt(0)
	s_barrier
	s_waitcnt lgkmcnt(0)
	v_mfma_f32_16x16x32_bf16 v[80:83], v[154:157], v[202:205], v[80:83]
	v_mfma_f32_16x16x32_bf16 v[72:75], v[172:175], v[202:205], v[72:75]
	v_mfma_f32_16x16x32_bf16 v[64:67], v[154:157], v[210:213], v[64:67]
	v_mfma_f32_16x16x32_bf16 v[56:59], v[172:175], v[210:213], v[56:59]
	v_mfma_f32_16x16x32_bf16 v[48:51], v[154:157], v[218:221], v[48:51]
	v_mfma_f32_16x16x32_bf16 v[40:43], v[172:175], v[218:221], v[40:43]
	v_mfma_f32_16x16x32_bf16 v[32:35], v[154:157], v[226:229], v[32:35]
	v_mfma_f32_16x16x32_bf16 v[24:27], v[172:175], v[226:229], v[24:27]
	v_mfma_f32_16x16x32_bf16 v[80:83], v[168:171], v[206:209], v[80:83]
	v_mfma_f32_16x16x32_bf16 v[72:75], v[176:179], v[206:209], v[72:75]
	v_mfma_f32_16x16x32_bf16 v[64:67], v[168:171], v[214:217], v[64:67]
	v_mfma_f32_16x16x32_bf16 v[56:59], v[176:179], v[214:217], v[56:59]
	v_mfma_f32_16x16x32_bf16 v[48:51], v[168:171], v[222:225], v[48:51]
	v_mfma_f32_16x16x32_bf16 v[40:43], v[176:179], v[222:225], v[40:43]
	v_mfma_f32_16x16x32_bf16 v[32:35], v[168:171], v[236:239], v[32:35]
	v_mfma_f32_16x16x32_bf16 v[24:27], v[176:179], v[236:239], v[24:27]
	v_mfma_f32_16x16x32_bf16 v[76:79], v[180:183], v[202:205], v[76:79]
	v_mfma_f32_16x16x32_bf16 v[68:71], v[188:191], v[202:205], v[68:71]
	v_mfma_f32_16x16x32_bf16 v[60:63], v[180:183], v[210:213], v[60:63]
	v_mfma_f32_16x16x32_bf16 v[52:55], v[188:191], v[210:213], v[52:55]
	v_mfma_f32_16x16x32_bf16 v[44:47], v[180:183], v[218:221], v[44:47]
	v_mfma_f32_16x16x32_bf16 v[36:39], v[188:191], v[218:221], v[36:39]
	v_mfma_f32_16x16x32_bf16 v[28:31], v[180:183], v[226:229], v[28:31]
	v_mfma_f32_16x16x32_bf16 v[20:23], v[188:191], v[226:229], v[20:23]
	v_mfma_f32_16x16x32_bf16 v[76:79], v[184:187], v[206:209], v[76:79]
	v_mfma_f32_16x16x32_bf16 v[68:71], v[198:201], v[206:209], v[68:71]
	v_mfma_f32_16x16x32_bf16 v[60:63], v[184:187], v[214:217], v[60:63]
	v_mfma_f32_16x16x32_bf16 v[52:55], v[198:201], v[214:217], v[52:55]
	v_mfma_f32_16x16x32_bf16 v[44:47], v[184:187], v[222:225], v[44:47]
	v_mfma_f32_16x16x32_bf16 v[36:39], v[198:201], v[222:225], v[36:39]
	v_mfma_f32_16x16x32_bf16 v[28:31], v[184:187], v[236:239], v[28:31]
	v_mfma_f32_16x16x32_bf16 v[20:23], v[198:201], v[236:239], v[20:23]
	s_barrier
	v_add_u32_e32 v167, s48, v163
	ds_read_b128 v[154:157], v167
	ds_read_b128 v[168:171], v167 offset:1024
	ds_read_b128 v[172:175], v167 offset:2048
	ds_read_b128 v[176:179], v167 offset:3072
	v_add_u32_e32 v167, s54, v163
	ds_read_b128 v[180:183], v167
	ds_read_b128 v[184:187], v167 offset:1024
	ds_read_b128 v[188:191], v167 offset:2048
	ds_read_b128 v[198:201], v167 offset:3072
	s_add_u32 s68, s28, 0x40000
	s_addc_u32 s69, s29, 0
	s_mov_b32 m0, s46
	v_lshl_add_u64 v[242:243], s[68:69], 0, v[148:149]
	ds_read_b128 v[202:205], v166 offset:32768
	ds_read_b128 v[206:209], v166 offset:33792
	ds_read_b128 v[210:213], v166 offset:34816
	ds_read_b128 v[214:217], v166 offset:35840
	ds_read_b128 v[218:221], v166 offset:36864
	ds_read_b128 v[222:225], v166 offset:37888
	ds_read_b128 v[226:229], v166 offset:38912
	ds_read_b128 v[236:239], v166 offset:39936
	global_load_lds_dwordx4 v[242:243], off
	v_lshl_add_u64 v[242:243], s[68:69], 0, v[150:151]
	s_mov_b32 m0, s47
	s_nop 0
	global_load_lds_dwordx4 v[242:243], off
	s_waitcnt vmcnt(16)
	s_cmp_lg_u32 s67, 0
	s_cbranch_scc1 .Lpg8f14
	s_waitcnt vmcnt(8)
.Lpg8f14:
	s_waitcnt lgkmcnt(0)
	s_barrier
	s_waitcnt lgkmcnt(0)
	v_mfma_f32_16x16x32_bf16 v[144:147], v[154:157], v[202:205], v[144:147]
	v_mfma_f32_16x16x32_bf16 v[136:139], v[172:175], v[202:205], v[136:139]
	v_mfma_f32_16x16x32_bf16 v[128:131], v[154:157], v[210:213], v[128:131]
	v_mfma_f32_16x16x32_bf16 v[120:123], v[172:175], v[210:213], v[120:123]
	v_mfma_f32_16x16x32_bf16 v[112:115], v[154:157], v[218:221], v[112:115]
	v_mfma_f32_16x16x32_bf16 v[104:107], v[172:175], v[218:221], v[104:107]
	v_mfma_f32_16x16x32_bf16 v[96:99], v[154:157], v[226:229], v[96:99]
	v_mfma_f32_16x16x32_bf16 v[88:91], v[172:175], v[226:229], v[88:91]
	v_mfma_f32_16x16x32_bf16 v[144:147], v[168:171], v[206:209], v[144:147]
	v_mfma_f32_16x16x32_bf16 v[136:139], v[176:179], v[206:209], v[136:139]
	v_mfma_f32_16x16x32_bf16 v[128:131], v[168:171], v[214:217], v[128:131]
	v_mfma_f32_16x16x32_bf16 v[120:123], v[176:179], v[214:217], v[120:123]
	v_mfma_f32_16x16x32_bf16 v[112:115], v[168:171], v[222:225], v[112:115]
	v_mfma_f32_16x16x32_bf16 v[104:107], v[176:179], v[222:225], v[104:107]
	v_mfma_f32_16x16x32_bf16 v[96:99], v[168:171], v[236:239], v[96:99]
	v_mfma_f32_16x16x32_bf16 v[88:91], v[176:179], v[236:239], v[88:91]
	v_mfma_f32_16x16x32_bf16 v[140:143], v[180:183], v[202:205], v[140:143]
	v_mfma_f32_16x16x32_bf16 v[132:135], v[188:191], v[202:205], v[132:135]
	v_mfma_f32_16x16x32_bf16 v[124:127], v[180:183], v[210:213], v[124:127]
	v_mfma_f32_16x16x32_bf16 v[116:119], v[188:191], v[210:213], v[116:119]
	v_mfma_f32_16x16x32_bf16 v[108:111], v[180:183], v[218:221], v[108:111]
	v_mfma_f32_16x16x32_bf16 v[100:103], v[188:191], v[218:221], v[100:103]
	v_mfma_f32_16x16x32_bf16 v[92:95], v[180:183], v[226:229], v[92:95]
	v_mfma_f32_16x16x32_bf16 v[84:87], v[188:191], v[226:229], v[84:87]
	v_mfma_f32_16x16x32_bf16 v[140:143], v[184:187], v[206:209], v[140:143]
	v_mfma_f32_16x16x32_bf16 v[132:135], v[198:201], v[206:209], v[132:135]
	v_mfma_f32_16x16x32_bf16 v[124:127], v[184:187], v[214:217], v[124:127]
	v_mfma_f32_16x16x32_bf16 v[116:119], v[198:201], v[214:217], v[116:119]
	v_mfma_f32_16x16x32_bf16 v[108:111], v[184:187], v[222:225], v[108:111]
	v_mfma_f32_16x16x32_bf16 v[100:103], v[198:201], v[222:225], v[100:103]
	v_mfma_f32_16x16x32_bf16 v[92:95], v[184:187], v[236:239], v[92:95]
	v_mfma_f32_16x16x32_bf16 v[84:87], v[198:201], v[236:239], v[84:87]
	s_barrier
	s_mov_b32 m0, s50
	v_lshl_add_u64 v[158:159], v[158:159], 0, s[86:87]
	s_add_u32 s30, s30, 0x40080
	ds_read_b128 v[202:205], v166 offset:49152
	ds_read_b128 v[206:209], v166 offset:50176
	ds_read_b128 v[210:213], v166 offset:51200
	ds_read_b128 v[214:217], v166 offset:52224
	ds_read_b128 v[218:221], v166 offset:53248
	ds_read_b128 v[222:225], v166 offset:54272
	ds_read_b128 v[226:229], v166 offset:55296
	ds_read_b128 v[236:239], v166 offset:56320
	global_load_lds_dwordx4 v[158:159], off
	v_lshl_add_u64 v[158:159], v[194:195], 0, s[86:87]
	s_mov_b32 m0, s51
	s_addc_u32 s31, s31, 0
	global_load_lds_dwordx4 v[158:159], off
	v_lshl_add_u64 v[158:159], s[30:31], 0, v[2:3]
	s_mov_b32 m0, s55
	s_nop 0
	global_load_lds_dwordx4 v[158:159], off
	v_lshl_add_u64 v[158:159], s[30:31], 0, v[152:153]
	s_mov_b32 m0, s56
	s_nop 0
	global_load_lds_dwordx4 v[158:159], off
	v_lshl_add_u64 v[158:159], v[230:231], 0, s[86:87]
	s_mov_b32 m0, s52
	s_nop 0
	global_load_lds_dwordx4 v[158:159], off
	v_lshl_add_u64 v[158:159], v[240:241], 0, s[86:87]
	s_mov_b32 m0, s53
	s_nop 0
	global_load_lds_dwordx4 v[158:159], off
	s_waitcnt vmcnt(8)
	s_waitcnt lgkmcnt(0)
	s_barrier
	s_waitcnt lgkmcnt(0)
	v_mfma_f32_16x16x32_bf16 v[80:83], v[154:157], v[202:205], v[80:83]
	v_mfma_f32_16x16x32_bf16 v[72:75], v[172:175], v[202:205], v[72:75]
	v_mfma_f32_16x16x32_bf16 v[64:67], v[154:157], v[210:213], v[64:67]
	v_mfma_f32_16x16x32_bf16 v[56:59], v[172:175], v[210:213], v[56:59]
	v_mfma_f32_16x16x32_bf16 v[48:51], v[154:157], v[218:221], v[48:51]
	v_mfma_f32_16x16x32_bf16 v[40:43], v[172:175], v[218:221], v[40:43]
	v_mfma_f32_16x16x32_bf16 v[32:35], v[154:157], v[226:229], v[32:35]
	v_mfma_f32_16x16x32_bf16 v[24:27], v[172:175], v[226:229], v[24:27]
	v_mfma_f32_16x16x32_bf16 v[80:83], v[168:171], v[206:209], v[80:83]
	v_mfma_f32_16x16x32_bf16 v[72:75], v[176:179], v[206:209], v[72:75]
	v_mfma_f32_16x16x32_bf16 v[64:67], v[168:171], v[214:217], v[64:67]
	v_mfma_f32_16x16x32_bf16 v[56:59], v[176:179], v[214:217], v[56:59]
	v_mfma_f32_16x16x32_bf16 v[48:51], v[168:171], v[222:225], v[48:51]
	v_mfma_f32_16x16x32_bf16 v[40:43], v[176:179], v[222:225], v[40:43]
	v_mfma_f32_16x16x32_bf16 v[32:35], v[168:171], v[236:239], v[32:35]
	v_mfma_f32_16x16x32_bf16 v[24:27], v[176:179], v[236:239], v[24:27]
	v_mfma_f32_16x16x32_bf16 v[76:79], v[180:183], v[202:205], v[76:79]
	v_mfma_f32_16x16x32_bf16 v[68:71], v[188:191], v[202:205], v[68:71]
	v_mfma_f32_16x16x32_bf16 v[60:63], v[180:183], v[210:213], v[60:63]
	v_mfma_f32_16x16x32_bf16 v[52:55], v[188:191], v[210:213], v[52:55]
	v_mfma_f32_16x16x32_bf16 v[44:47], v[180:183], v[218:221], v[44:47]
	v_mfma_f32_16x16x32_bf16 v[36:39], v[188:191], v[218:221], v[36:39]
	v_mfma_f32_16x16x32_bf16 v[28:31], v[180:183], v[226:229], v[28:31]
	v_mfma_f32_16x16x32_bf16 v[20:23], v[188:191], v[226:229], v[20:23]
	v_mfma_f32_16x16x32_bf16 v[76:79], v[184:187], v[206:209], v[76:79]
	v_mfma_f32_16x16x32_bf16 v[68:71], v[198:201], v[206:209], v[68:71]
	v_mfma_f32_16x16x32_bf16 v[60:63], v[184:187], v[214:217], v[60:63]
	v_mfma_f32_16x16x32_bf16 v[52:55], v[198:201], v[214:217], v[52:55]
	v_mfma_f32_16x16x32_bf16 v[44:47], v[184:187], v[222:225], v[44:47]
	v_mfma_f32_16x16x32_bf16 v[36:39], v[198:201], v[222:225], v[36:39]
	v_mfma_f32_16x16x32_bf16 v[28:31], v[184:187], v[236:239], v[28:31]
	v_mfma_f32_16x16x32_bf16 v[20:23], v[198:201], v[236:239], v[20:23]
	s_barrier
	s_add_u32 s28, s28, 0x40080
	s_addc_u32 s29, s29, 0
	s_mov_b32 m0, s57
	v_lshl_add_u64 v[154:155], s[28:29], 0, v[148:149]
	global_load_lds_dwordx4 v[154:155], off
	v_lshl_add_u64 v[154:155], s[28:29], 0, v[150:151]
	s_mov_b32 m0, s58
	s_nop 0
	global_load_lds_dwordx4 v[154:155], off
	s_add_i32 s66, s66, 2
	s_add_u32 s21, s21, 0x100
	s_addc_u32 s23, s23, 0
	s_add_u32 s63, s63, 0x100
	s_addc_u32 s65, s65, 0
	s_cmp_gt_u32 s66, 13
	s_cbranch_scc0 .LBB0_2252
	s_and_b64 vcc, exec, s[18:19]
	s_cbranch_vccz .LBB0_2255
	s_barrier

.Lpg8f15:
	s_waitcnt lgkmcnt(0)
	s_barrier
	s_waitcnt lgkmcnt(0)
	v_mfma_f32_16x16x32_bf16 v[148:151], v[100:103], v[164:167], v[148:151]
	v_mfma_f32_16x16x32_bf16 v[144:147], v[116:119], v[164:167], v[144:147]
	v_mfma_f32_16x16x32_bf16 v[124:127], v[100:103], v[172:175], v[124:127]
	v_mfma_f32_16x16x32_bf16 v[120:123], v[116:119], v[172:175], v[120:123]
	v_mfma_f32_16x16x32_bf16 v[96:99], v[100:103], v[180:183], v[96:99]
	v_mfma_f32_16x16x32_bf16 v[92:95], v[116:119], v[180:183], v[92:95]
	v_mfma_f32_16x16x32_bf16 v[80:83], v[100:103], v[188:191], v[80:83]
	v_mfma_f32_16x16x32_bf16 v[76:79], v[116:119], v[188:191], v[76:79]
	v_mfma_f32_16x16x32_bf16 v[148:151], v[104:107], v[168:171], v[148:151]
	v_mfma_f32_16x16x32_bf16 v[144:147], v[128:131], v[168:171], v[144:147]
	v_mfma_f32_16x16x32_bf16 v[124:127], v[104:107], v[176:179], v[124:127]
	v_mfma_f32_16x16x32_bf16 v[120:123], v[128:131], v[176:179], v[120:123]
	v_mfma_f32_16x16x32_bf16 v[96:99], v[104:107], v[184:187], v[96:99]
	v_mfma_f32_16x16x32_bf16 v[92:95], v[128:131], v[184:187], v[92:95]
	v_mfma_f32_16x16x32_bf16 v[80:83], v[104:107], v[204:207], v[80:83]
	v_mfma_f32_16x16x32_bf16 v[76:79], v[128:131], v[204:207], v[76:79]
	v_mfma_f32_16x16x32_bf16 v[136:139], v[140:143], v[164:167], v[136:139]
	v_mfma_f32_16x16x32_bf16 v[132:135], v[156:159], v[164:167], v[132:135]
	v_mfma_f32_16x16x32_bf16 v[112:115], v[140:143], v[172:175], v[112:115]
	v_mfma_f32_16x16x32_bf16 v[108:111], v[156:159], v[172:175], v[108:111]
	v_mfma_f32_16x16x32_bf16 v[88:91], v[140:143], v[180:183], v[88:91]
	v_mfma_f32_16x16x32_bf16 v[84:87], v[156:159], v[180:183], v[84:87]
	v_mfma_f32_16x16x32_bf16 v[72:75], v[140:143], v[188:191], v[72:75]
	v_mfma_f32_16x16x32_bf16 v[68:71], v[156:159], v[188:191], v[68:71]
	v_mfma_f32_16x16x32_bf16 v[136:139], v[152:155], v[168:171], v[136:139]
	v_mfma_f32_16x16x32_bf16 v[132:135], v[160:163], v[168:171], v[132:135]
	v_mfma_f32_16x16x32_bf16 v[112:115], v[152:155], v[176:179], v[112:115]
	v_mfma_f32_16x16x32_bf16 v[108:111], v[160:163], v[176:179], v[108:111]
	v_mfma_f32_16x16x32_bf16 v[88:91], v[152:155], v[184:187], v[88:91]
	v_mfma_f32_16x16x32_bf16 v[84:87], v[160:163], v[184:187], v[84:87]
	v_mfma_f32_16x16x32_bf16 v[72:75], v[152:155], v[204:207], v[72:75]
	v_mfma_f32_16x16x32_bf16 v[68:71], v[160:163], v[204:207], v[68:71]
	s_barrier
	s_mov_b32 m0, s40
	v_lshl_add_u64 v[194:195], s[30:31], 0, v[2:3]
	s_add_u32 s72, s30, 0xb0000
	ds_read_b128 v[164:167], v236 offset:16384
	ds_read_b128 v[168:171], v236 offset:17408
	ds_read_b128 v[172:175], v236 offset:18432
	ds_read_b128 v[176:179], v236 offset:19456
	ds_read_b128 v[180:183], v236 offset:20480
	ds_read_b128 v[184:187], v236 offset:21504
	ds_read_b128 v[188:191], v236 offset:22528
	ds_read_b128 v[204:207], v236 offset:23552
	global_load_lds_dwordx4 v[194:195], off
	v_lshl_add_u64 v[208:209], s[30:31], 0, v[198:199]
	s_mov_b32 m0, s41
	s_addc_u32 s73, s31, 0
	global_load_lds_dwordx4 v[208:209], off
	v_lshl_add_u64 v[210:211], s[72:73], 0, v[2:3]
	s_mov_b32 m0, s44
	v_lshl_add_u64 v[212:213], s[14:15], 0, v[200:201]
	global_load_lds_dwordx4 v[210:211], off
	v_lshl_add_u64 v[210:211], s[72:73], 0, v[198:199]
	s_mov_b32 m0, s45
	s_nop 0
	global_load_lds_dwordx4 v[210:211], off
	v_lshl_add_u64 v[210:211], s[14:15], 0, v[202:203]
	s_mov_b32 m0, s46
	s_nop 0
	global_load_lds_dwordx4 v[210:211], off
	s_mov_b32 m0, s47
	s_nop 0
	global_load_lds_dwordx4 v[212:213], off
	s_waitcnt vmcnt(40)
	s_cmp_lg_u32 s71, 0
	s_cbranch_scc1 .Lpg8f16
	s_waitcnt vmcnt(8)
.Lpg8f16:
	s_waitcnt lgkmcnt(0)
	s_barrier
	s_waitcnt lgkmcnt(0)
	v_mfma_f32_16x16x32_bf16 v[64:67], v[100:103], v[164:167], v[64:67]
	v_mfma_f32_16x16x32_bf16 v[60:63], v[116:119], v[164:167], v[60:63]
	v_mfma_f32_16x16x32_bf16 v[48:51], v[100:103], v[172:175], v[48:51]
	v_mfma_f32_16x16x32_bf16 v[44:47], v[116:119], v[172:175], v[44:47]
	v_mfma_f32_16x16x32_bf16 v[32:35], v[100:103], v[180:183], v[32:35]
	v_mfma_f32_16x16x32_bf16 v[28:31], v[116:119], v[180:183], v[28:31]
	v_mfma_f32_16x16x32_bf16 v[16:19], v[100:103], v[188:191], v[16:19]
	v_mfma_f32_16x16x32_bf16 v[12:15], v[116:119], v[188:191], v[12:15]
	v_mfma_f32_16x16x32_bf16 v[64:67], v[104:107], v[168:171], v[64:67]
	v_mfma_f32_16x16x32_bf16 v[60:63], v[128:131], v[168:171], v[60:63]
	v_mfma_f32_16x16x32_bf16 v[48:51], v[104:107], v[176:179], v[48:51]
	v_mfma_f32_16x16x32_bf16 v[44:47], v[128:131], v[176:179], v[44:47]
	v_mfma_f32_16x16x32_bf16 v[32:35], v[104:107], v[184:187], v[32:35]
	v_mfma_f32_16x16x32_bf16 v[28:31], v[128:131], v[184:187], v[28:31]
	v_mfma_f32_16x16x32_bf16 v[16:19], v[104:107], v[204:207], v[16:19]
	v_mfma_f32_16x16x32_bf16 v[12:15], v[128:131], v[204:207], v[12:15]
	v_mfma_f32_16x16x32_bf16 v[56:59], v[140:143], v[164:167], v[56:59]
	v_mfma_f32_16x16x32_bf16 v[52:55], v[156:159], v[164:167], v[52:55]
	v_mfma_f32_16x16x32_bf16 v[40:43], v[140:143], v[172:175], v[40:43]
	v_mfma_f32_16x16x32_bf16 v[36:39], v[156:159], v[172:175], v[36:39]
	v_mfma_f32_16x16x32_bf16 v[24:27], v[140:143], v[180:183], v[24:27]
	v_mfma_f32_16x16x32_bf16 v[20:23], v[156:159], v[180:183], v[20:23]
	v_mfma_f32_16x16x32_bf16 v[8:11], v[140:143], v[188:191], v[8:11]
	v_mfma_f32_16x16x32_bf16 v[4:7], v[156:159], v[188:191], v[4:7]
	v_mfma_f32_16x16x32_bf16 v[56:59], v[152:155], v[168:171], v[56:59]
	v_mfma_f32_16x16x32_bf16 v[52:55], v[160:163], v[168:171], v[52:55]
	v_mfma_f32_16x16x32_bf16 v[40:43], v[152:155], v[176:179], v[40:43]
	v_mfma_f32_16x16x32_bf16 v[36:39], v[160:163], v[176:179], v[36:39]
	v_mfma_f32_16x16x32_bf16 v[24:27], v[152:155], v[184:187], v[24:27]
	v_mfma_f32_16x16x32_bf16 v[20:23], v[160:163], v[184:187], v[20:23]
	v_mfma_f32_16x16x32_bf16 v[8:11], v[152:155], v[204:207], v[8:11]
	v_mfma_f32_16x16x32_bf16 v[4:7], v[160:163], v[204:207], v[4:7]
	s_barrier
	v_add_u32_e32 v128, s53, v230
	v_add_u32_e32 v160, s58, v230
	ds_read_b128 v[100:103], v128
	ds_read_b128 v[104:107], v128 offset:1024
	ds_read_b128 v[116:119], v128 offset:2048
	ds_read_b128 v[128:131], v128 offset:3072
	ds_read_b128 v[140:143], v160
	ds_read_b128 v[152:155], v160 offset:1024
	ds_read_b128 v[156:159], v160 offset:2048
	ds_read_b128 v[160:163], v160 offset:3072
	s_add_u32 s72, s14, 0xb0000
	s_addc_u32 s73, s15, 0
	s_mov_b32 m0, s50
	v_lshl_add_u64 v[214:215], s[72:73], 0, v[202:203]
	ds_read_b128 v[164:167], v236 offset:32768
	ds_read_b128 v[168:171], v236 offset:33792
	ds_read_b128 v[172:175], v236 offset:34816
	ds_read_b128 v[176:179], v236 offset:35840
	ds_read_b128 v[180:183], v236 offset:36864
	ds_read_b128 v[184:187], v236 offset:37888
	ds_read_b128 v[188:191], v236 offset:38912
	ds_read_b128 v[204:207], v236 offset:39936
	global_load_lds_dwordx4 v[214:215], off
	v_lshl_add_u64 v[214:215], s[72:73], 0, v[200:201]
	s_mov_b32 m0, s51
	s_nop 0
	global_load_lds_dwordx4 v[214:215], off
	s_waitcnt vmcnt(40)
	s_cmp_lg_u32 s71, 0
	s_cbranch_scc1 .Lpg8f17
	s_waitcnt vmcnt(8)
.Lpg8f17:
	s_waitcnt lgkmcnt(0)
	s_barrier
	s_waitcnt lgkmcnt(0)
	v_mfma_f32_16x16x32_bf16 v[148:151], v[100:103], v[164:167], v[148:151]
	v_mfma_f32_16x16x32_bf16 v[144:147], v[116:119], v[164:167], v[144:147]
	v_mfma_f32_16x16x32_bf16 v[124:127], v[100:103], v[172:175], v[124:127]
	v_mfma_f32_16x16x32_bf16 v[120:123], v[116:119], v[172:175], v[120:123]
	v_mfma_f32_16x16x32_bf16 v[96:99], v[100:103], v[180:183], v[96:99]
	v_mfma_f32_16x16x32_bf16 v[92:95], v[116:119], v[180:183], v[92:95]
	v_mfma_f32_16x16x32_bf16 v[80:83], v[100:103], v[188:191], v[80:83]
	v_mfma_f32_16x16x32_bf16 v[76:79], v[116:119], v[188:191], v[76:79]
	v_mfma_f32_16x16x32_bf16 v[148:151], v[104:107], v[168:171], v[148:151]
	v_mfma_f32_16x16x32_bf16 v[144:147], v[128:131], v[168:171], v[144:147]
	v_mfma_f32_16x16x32_bf16 v[124:127], v[104:107], v[176:179], v[124:127]
	v_mfma_f32_16x16x32_bf16 v[120:123], v[128:131], v[176:179], v[120:123]
	v_mfma_f32_16x16x32_bf16 v[96:99], v[104:107], v[184:187], v[96:99]
	v_mfma_f32_16x16x32_bf16 v[92:95], v[128:131], v[184:187], v[92:95]
	v_mfma_f32_16x16x32_bf16 v[80:83], v[104:107], v[204:207], v[80:83]
	v_mfma_f32_16x16x32_bf16 v[76:79], v[128:131], v[204:207], v[76:79]
	v_mfma_f32_16x16x32_bf16 v[136:139], v[140:143], v[164:167], v[136:139]
	v_mfma_f32_16x16x32_bf16 v[132:135], v[156:159], v[164:167], v[132:135]
	v_mfma_f32_16x16x32_bf16 v[112:115], v[140:143], v[172:175], v[112:115]
	v_mfma_f32_16x16x32_bf16 v[108:111], v[156:159], v[172:175], v[108:111]
	v_mfma_f32_16x16x32_bf16 v[88:91], v[140:143], v[180:183], v[88:91]
	v_mfma_f32_16x16x32_bf16 v[84:87], v[156:159], v[180:183], v[84:87]
	v_mfma_f32_16x16x32_bf16 v[72:75], v[140:143], v[188:191], v[72:75]
	v_mfma_f32_16x16x32_bf16 v[68:71], v[156:159], v[188:191], v[68:71]
	v_mfma_f32_16x16x32_bf16 v[136:139], v[152:155], v[168:171], v[136:139]
	v_mfma_f32_16x16x32_bf16 v[132:135], v[160:163], v[168:171], v[132:135]
	v_mfma_f32_16x16x32_bf16 v[112:115], v[152:155], v[176:179], v[112:115]
	v_mfma_f32_16x16x32_bf16 v[108:111], v[160:163], v[176:179], v[108:111]
	v_mfma_f32_16x16x32_bf16 v[88:91], v[152:155], v[184:187], v[88:91]
	v_mfma_f32_16x16x32_bf16 v[84:87], v[160:163], v[184:187], v[84:87]
	v_mfma_f32_16x16x32_bf16 v[72:75], v[152:155], v[204:207], v[72:75]
	v_mfma_f32_16x16x32_bf16 v[68:71], v[160:163], v[204:207], v[68:71]
	s_barrier
	s_mov_b32 m0, s54
	v_lshl_add_u64 v[194:195], v[194:195], 0, s[86:87]
	s_add_u32 s30, s30, 0xb0080
	ds_read_b128 v[164:167], v236 offset:49152
	ds_read_b128 v[168:171], v236 offset:50176
	ds_read_b128 v[172:175], v236 offset:51200
	ds_read_b128 v[176:179], v236 offset:52224
	ds_read_b128 v[180:183], v236 offset:53248
	ds_read_b128 v[184:187], v236 offset:54272
	ds_read_b128 v[188:191], v236 offset:55296
	ds_read_b128 v[204:207], v236 offset:56320
	global_load_lds_dwordx4 v[194:195], off
	v_lshl_add_u64 v[194:195], v[208:209], 0, s[86:87]
	s_mov_b32 m0, s55
	s_addc_u32 s31, s31, 0
	global_load_lds_dwordx4 v[194:195], off
	v_lshl_add_u64 v[194:195], s[30:31], 0, v[2:3]
	s_mov_b32 m0, s59
	s_nop 0
	global_load_lds_dwordx4 v[194:195], off
	v_lshl_add_u64 v[194:195], s[30:31], 0, v[198:199]
	s_mov_b32 m0, s60
	s_nop 0
	global_load_lds_dwordx4 v[194:195], off
	v_lshl_add_u64 v[194:195], v[210:211], 0, s[86:87]
	s_mov_b32 m0, s56
	s_nop 0
	global_load_lds_dwordx4 v[194:195], off
	v_lshl_add_u64 v[194:195], v[212:213], 0, s[86:87]
	s_mov_b32 m0, s57
	s_nop 0
	global_load_lds_dwordx4 v[194:195], off
	s_waitcnt vmcnt(8)
	s_waitcnt lgkmcnt(0)
	s_barrier
	s_waitcnt lgkmcnt(0)
	v_mfma_f32_16x16x32_bf16 v[64:67], v[100:103], v[164:167], v[64:67]
	v_mfma_f32_16x16x32_bf16 v[60:63], v[116:119], v[164:167], v[60:63]
	v_mfma_f32_16x16x32_bf16 v[48:51], v[100:103], v[172:175], v[48:51]
	v_mfma_f32_16x16x32_bf16 v[44:47], v[116:119], v[172:175], v[44:47]
	v_mfma_f32_16x16x32_bf16 v[32:35], v[100:103], v[180:183], v[32:35]
	v_mfma_f32_16x16x32_bf16 v[28:31], v[116:119], v[180:183], v[28:31]
	v_mfma_f32_16x16x32_bf16 v[16:19], v[100:103], v[188:191], v[16:19]
	v_mfma_f32_16x16x32_bf16 v[12:15], v[116:119], v[188:191], v[12:15]
	v_mfma_f32_16x16x32_bf16 v[64:67], v[104:107], v[168:171], v[64:67]
	v_mfma_f32_16x16x32_bf16 v[60:63], v[128:131], v[168:171], v[60:63]
	v_mfma_f32_16x16x32_bf16 v[48:51], v[104:107], v[176:179], v[48:51]
	v_mfma_f32_16x16x32_bf16 v[44:47], v[128:131], v[176:179], v[44:47]
	v_mfma_f32_16x16x32_bf16 v[32:35], v[104:107], v[184:187], v[32:35]
	v_mfma_f32_16x16x32_bf16 v[28:31], v[128:131], v[184:187], v[28:31]
	v_mfma_f32_16x16x32_bf16 v[16:19], v[104:107], v[204:207], v[16:19]
	v_mfma_f32_16x16x32_bf16 v[12:15], v[128:131], v[204:207], v[12:15]
	v_mfma_f32_16x16x32_bf16 v[56:59], v[140:143], v[164:167], v[56:59]
	v_mfma_f32_16x16x32_bf16 v[52:55], v[156:159], v[164:167], v[52:55]
	v_mfma_f32_16x16x32_bf16 v[40:43], v[140:143], v[172:175], v[40:43]
	v_mfma_f32_16x16x32_bf16 v[36:39], v[156:159], v[172:175], v[36:39]
	v_mfma_f32_16x16x32_bf16 v[24:27], v[140:143], v[180:183], v[24:27]
	v_mfma_f32_16x16x32_bf16 v[20:23], v[156:159], v[180:183], v[20:23]
	v_mfma_f32_16x16x32_bf16 v[8:11], v[140:143], v[188:191], v[8:11]
	v_mfma_f32_16x16x32_bf16 v[4:7], v[156:159], v[188:191], v[4:7]
	v_mfma_f32_16x16x32_bf16 v[56:59], v[152:155], v[168:171], v[56:59]
	v_mfma_f32_16x16x32_bf16 v[52:55], v[160:163], v[168:171], v[52:55]
	v_mfma_f32_16x16x32_bf16 v[40:43], v[152:155], v[176:179], v[40:43]
	v_mfma_f32_16x16x32_bf16 v[36:39], v[160:163], v[176:179], v[36:39]
	v_mfma_f32_16x16x32_bf16 v[24:27], v[152:155], v[184:187], v[24:27]
	v_mfma_f32_16x16x32_bf16 v[20:23], v[160:163], v[184:187], v[20:23]
	v_mfma_f32_16x16x32_bf16 v[8:11], v[152:155], v[204:207], v[8:11]
	v_mfma_f32_16x16x32_bf16 v[4:7], v[160:163], v[204:207], v[4:7]
	s_barrier
	s_add_u32 s14, s14, 0xb0080
	s_addc_u32 s15, s15, 0
	s_mov_b32 m0, s61
	v_lshl_add_u64 v[100:101], s[14:15], 0, v[202:203]
	global_load_lds_dwordx4 v[100:101], off
	v_lshl_add_u64 v[100:101], s[14:15], 0, v[200:201]
	s_mov_b32 m0, s62
	s_nop 0
	global_load_lds_dwordx4 v[100:101], off
	s_add_i32 s70, s70, 2
	s_add_u32 s34, s34, 0x100
	s_addc_u32 s35, s35, 0
	s_add_u32 s68, s68, 0x100
	s_addc_u32 s69, s69, 0
	s_cmp_gt_u32 s70, 41
	s_cbranch_scc0 .LBB0_2329
	s_and_b64 vcc, exec, s[22:23]
	s_cbranch_vccz .LBB0_2332
	s_barrier
